# batched/prefetched serialized loads in GEMM epilogues, gather setup, scan-A prefetch, router and combine norm vectors, LDS fill loops; DPP reductions
# speedup vs baseline: 1.0467x; 1.0262x over previous
.LBB0_235:
	s_mov_b64 s[4:5], s[84:85]
	s_andn2_b64 vcc, exec, s[0:1]
	s_mov_b64 s[6:7], s[86:87]
	s_mov_b64 s[0:1], s[80:81]
	v_writelane_b32 v255, s0, 40
	s_nop 1
	v_writelane_b32 v255, s1, 41
	v_writelane_b32 v255, s2, 42
	v_writelane_b32 v255, s3, 43
	v_writelane_b32 v255, s4, 44
	v_writelane_b32 v255, s5, 45
	v_writelane_b32 v255, s6, 46
	v_writelane_b32 v255, s7, 47
	s_cbranch_vccnz .LBB0_303
	v_mov_b32_e32 v2, v0
	s_movk_i32 s0, 0x800
	s_nop 0
	v_cmp_gt_i32_e32 vcc, s0, v2
	v_ashrrev_i32_e32 v3, 31, v2
	v_add_u32_e32 v1, 0xfffffe00, v2
	v_lshlrev_b32_e32 v4, 2, v2
	s_and_saveexec_b64 s[0:1], vcc
	s_cbranch_execz .LBB0_239
	v_readlane_b32 s2, v255, 37
	v_readlane_b32 s3, v255, 38
	s_lshl_b64 s[2:3], s[2:3], 15
	v_readlane_b32 s36, v252, 32
	v_readlane_b32 s37, v252, 33
	s_add_u32 s2, s36, s2
	s_addc_u32 s3, s37, s3
	s_add_i32 s4, 0, 0x2000
	v_add_u32_e32 v5, 0xfffffe00, v2
	v_lshl_add_u32 v8, v2, 4, s4
	v_lshlrev_b32_e32 v6, 2, v2
	s_mov_b64 s[4:5], 0
	v_readlane_b32 s38, v252, 34
	v_readlane_b32 s39, v252, 35
	v_readlane_b32 s40, v252, 36
	v_readlane_b32 s41, v252, 37
	v_readlane_b32 s42, v252, 38
	v_readlane_b32 s43, v252, 39
	v_readlane_b32 s44, v252, 40
	v_readlane_b32 s45, v252, 41
	v_readlane_b32 s46, v252, 42
	v_readlane_b32 s47, v252, 43
	v_readlane_b32 s48, v252, 44
	v_readlane_b32 s49, v252, 45
	v_readlane_b32 s50, v252, 46
	v_readlane_b32 s51, v252, 47
	v_ashrrev_i32_e32 v7, 31, v6
	v_lshl_add_u64 v[72:73], v[6:7], 2, s[2:3]
	s_mov_b64 s[4:5], 0x2000
	global_load_dwordx4 v[40:43], v[72:73], off
	v_lshl_add_u64 v[72:73], v[72:73], 0, s[4:5]
	global_load_dwordx4 v[44:47], v[72:73], off
	v_lshl_add_u64 v[72:73], v[72:73], 0, s[4:5]
	global_load_dwordx4 v[48:51], v[72:73], off
	v_lshl_add_u64 v[72:73], v[72:73], 0, s[4:5]
	global_load_dwordx4 v[52:55], v[72:73], off
	s_waitcnt vmcnt(0)
	ds_write_b128 v8, v[40:43]
	ds_write_b128 v8, v[44:47] offset:8192
	ds_write_b128 v8, v[48:51] offset:16384
	ds_write_b128 v8, v[52:55] offset:24576
.LBB0_239:
	s_or_b64 exec, exec, s[0:1]
	s_movk_i32 s0, 0x1000
	s_movk_i32 s6, 0xdff
	s_mov_b64 s[26:27], 0x1000
	v_cmp_gt_i32_e32 vcc, s0, v2
	s_and_saveexec_b64 s[0:1], vcc
	s_cbranch_execz .LBB0_242
	v_readlane_b32 s2, v255, 37
	v_readlane_b32 s3, v255, 38
	v_readlane_b32 s36, v252, 16
	s_lshl_b64 s[2:3], s[2:3], 16
	v_readlane_b32 s48, v252, 28
	v_readlane_b32 s49, v252, 29
	s_add_u32 s2, s48, s2
	s_addc_u32 s3, s49, s3
	s_add_i32 s4, 0, 0xa000
	v_add_u32_e32 v5, 0xfffffe00, v2
	v_lshl_add_u32 v8, v2, 4, s4
	v_lshlrev_b32_e32 v6, 2, v2
	s_mov_b64 s[4:5], 0
	v_readlane_b32 s37, v252, 17
	v_readlane_b32 s38, v252, 18
	v_readlane_b32 s39, v252, 19
	v_readlane_b32 s40, v252, 20
	v_readlane_b32 s41, v252, 21
	v_readlane_b32 s42, v252, 22
	v_readlane_b32 s43, v252, 23
	v_readlane_b32 s44, v252, 24
	v_readlane_b32 s45, v252, 25
	v_readlane_b32 s46, v252, 26
	v_readlane_b32 s47, v252, 27
	v_readlane_b32 s50, v252, 30
	v_readlane_b32 s51, v252, 31
	v_ashrrev_i32_e32 v7, 31, v6
	v_lshl_add_u64 v[72:73], v[6:7], 2, s[2:3]
	s_mov_b64 s[4:5], 0x2000
	global_load_dwordx4 v[40:43], v[72:73], off
	v_lshl_add_u64 v[72:73], v[72:73], 0, s[4:5]
	global_load_dwordx4 v[44:47], v[72:73], off
	v_lshl_add_u64 v[72:73], v[72:73], 0, s[4:5]
	global_load_dwordx4 v[48:51], v[72:73], off
	v_lshl_add_u64 v[72:73], v[72:73], 0, s[4:5]
	global_load_dwordx4 v[52:55], v[72:73], off
	v_lshl_add_u64 v[72:73], v[72:73], 0, s[4:5]
	global_load_dwordx4 v[56:59], v[72:73], off
	v_lshl_add_u64 v[72:73], v[72:73], 0, s[4:5]
	global_load_dwordx4 v[60:63], v[72:73], off
	v_lshl_add_u64 v[72:73], v[72:73], 0, s[4:5]
	global_load_dwordx4 v[64:67], v[72:73], off
	v_lshl_add_u64 v[72:73], v[72:73], 0, s[4:5]
	global_load_dwordx4 v[68:71], v[72:73], off
	s_waitcnt vmcnt(0)
	ds_write_b128 v8, v[40:43]
	ds_write_b128 v8, v[44:47] offset:8192
	ds_write_b128 v8, v[48:51] offset:16384
	ds_write_b128 v8, v[52:55] offset:24576
	ds_write_b128 v8, v[56:59] offset:32768
	ds_write_b128 v8, v[60:63] offset:40960
	ds_write_b128 v8, v[64:67] offset:49152
	ds_write_b128 v8, v[68:71] offset:57344
.LBB0_242:
	s_or_b64 exec, exec, s[0:1]
	v_readlane_b32 s0, v255, 37
	v_readlane_b32 s1, v255, 38
	s_lshl_b64 s[2:3], s[0:1], 14
	s_movk_i32 s0, 0x400
	v_cmp_gt_i32_e32 vcc, s0, v2
	s_and_saveexec_b64 s[0:1], vcc
	s_cbranch_execz .LBB0_245
	v_readlane_b32 s36, v252, 16
	v_readlane_b32 s38, v252, 18
	v_readlane_b32 s39, v252, 19
	s_add_u32 s4, s38, s2
	s_addc_u32 s5, s39, s3
	s_add_i32 s6, 0, 0x1a000
	v_lshl_add_u32 v6, v2, 4, s6
	s_mov_b64 s[6:7], 0
	v_readlane_b32 s37, v252, 17
	v_readlane_b32 s40, v252, 20
	v_readlane_b32 s41, v252, 21
	v_readlane_b32 s42, v252, 22
	v_readlane_b32 s43, v252, 23
	v_readlane_b32 s44, v252, 24
	v_readlane_b32 s45, v252, 25
	v_readlane_b32 s46, v252, 26
	v_readlane_b32 s47, v252, 27
	v_readlane_b32 s48, v252, 28
	v_readlane_b32 s49, v252, 29
	v_readlane_b32 s50, v252, 30
	v_readlane_b32 s51, v252, 31
	v_ashrrev_i32_e32 v5, 31, v4
	v_lshl_add_u64 v[72:73], v[4:5], 2, s[4:5]
	s_mov_b64 s[6:7], 0x2000
	global_load_dwordx4 v[40:43], v[72:73], off
	v_lshl_add_u64 v[72:73], v[72:73], 0, s[6:7]
	global_load_dwordx4 v[44:47], v[72:73], off
	s_waitcnt vmcnt(0)
	ds_write_b128 v6, v[40:43]
	ds_write_b128 v6, v[44:47] offset:8192

.LBB0_310:
	s_or_b64 exec, exec, s[0:1]
	s_waitcnt lgkmcnt(0)
	s_barrier
	ds_read_b128 v[26:29], v110 offset:27904
	ds_read_b128 v[30:33], v109 offset:42240
	s_mov_b64 s[0:1], 0x3c00
	s_mov_b32 s37, s22
	s_waitcnt lgkmcnt(0)
	v_mfma_f32_16x16x32_bf16 v[30:33], v[26:29], v[30:33], 0
	s_nop 7
	v_cvt_pk_bf16_f32 v30, v30, v31
	v_cvt_pk_bf16_f32 v31, v32, v33
	v_lshl_add_u64 v[32:33], v[54:55], 0, v[48:49]
	v_lshl_add_u64 v[54:55], v[32:33], 0, s[0:1]
	s_movk_i32 s0, 0x3000
	v_add_co_u32_e32 v32, vcc, s0, v32
	s_nop 1
	v_addc_co_u32_e32 v33, vcc, 0, v33, vcc
	global_store_dwordx2 v[32:33], v[30:31], off offset:3072
	ds_read_b128 v[30:33], v109 offset:43520
	s_waitcnt lgkmcnt(0)
	v_mfma_f32_16x16x32_bf16 v[30:33], v[26:29], v[30:33], 0
	s_and_b64 vcc, exec, s[8:9]
	s_nop 6
	v_cvt_pk_bf16_f32 v30, v30, v31
	v_cvt_pk_bf16_f32 v31, v32, v33
	global_store_dwordx2 v[54:55], v[30:31], off offset:512
	ds_read_b128 v[30:33], v109 offset:44800
	s_waitcnt lgkmcnt(0)
	v_mfma_f32_16x16x32_bf16 v[30:33], v[26:29], v[30:33], 0
	s_nop 7
	v_cvt_pk_bf16_f32 v30, v30, v31
	v_cvt_pk_bf16_f32 v31, v32, v33
	global_store_dwordx2 v[54:55], v[30:31], off offset:1024
	ds_read_b128 v[30:33], v109 offset:46080
	s_waitcnt lgkmcnt(0)
	v_mfma_f32_16x16x32_bf16 v[26:29], v[26:29], v[30:33], 0
	s_nop 7
	v_cvt_pk_bf16_f32 v26, v26, v27
	v_cvt_pk_bf16_f32 v27, v28, v29
	global_store_dwordx2 v[54:55], v[26:27], off offset:1536
	s_waitcnt lgkmcnt(0)
	s_barrier
	s_waitcnt vmcnt(4)
	v_lshlrev_b32_e32 v6, 16, v12
	v_lshlrev_b32_e32 v2, 16, v4
	v_and_b32_e32 v3, 0xffff0000, v4
	v_lshlrev_b32_e32 v4, 16, v5
	v_and_b32_e32 v5, 0xffff0000, v5
	v_and_b32_e32 v7, 0xffff0000, v12
	v_lshlrev_b32_e32 v8, 16, v13
	v_and_b32_e32 v9, 0xffff0000, v13
	v_lshlrev_b32_e32 v10, 16, v14
	v_and_b32_e32 v11, 0xffff0000, v14
	v_lshlrev_b32_e32 v12, 16, v15
	v_and_b32_e32 v13, 0xffff0000, v15
	v_lshlrev_b32_e32 v14, 16, v16
	v_and_b32_e32 v15, 0xffff0000, v16
	v_lshlrev_b32_e32 v16, 16, v17
	v_and_b32_e32 v17, 0xffff0000, v17
	v_lshlrev_b32_e32 v18, 16, v20
	v_and_b32_e32 v19, 0xffff0000, v20
	v_lshlrev_b32_e32 v20, 16, v21
	v_and_b32_e32 v21, 0xffff0000, v21
	v_lshlrev_b32_e32 v22, 16, v24
	v_and_b32_e32 v23, 0xffff0000, v24
	v_lshlrev_b32_e32 v24, 16, v25
	v_and_b32_e32 v25, 0xffff0000, v25
	s_cbranch_vccnz .LBB0_392
.LBB0_311:
	v_readlane_b32 s0, v255, 27
	ds_write_b128 v122, v[2:5]
	ds_write_b128 v122, v[6:9] offset:4096
	ds_write_b128 v122, v[10:13] offset:8192
	ds_write_b128 v122, v[14:17] offset:12288
	ds_write_b128 v122, v[18:21] offset:16384
	ds_write_b128 v122, v[22:25] offset:20480
	ds_write_b32 v111, v35 offset:37152
	ds_write_b32 v112, v35 offset:37152
	ds_write_b32 v113, v35 offset:42272
	ds_write_b32 v114, v35 offset:42272
	ds_write_b32 v115, v35 offset:47392
	ds_write_b32 v116, v35 offset:47392
	ds_write_b32 v71, v35 offset:52512
	s_add_i32 s22, s37, s0
	s_waitcnt lgkmcnt(0)
	s_barrier
	s_cmpk_gt_i32 s22, 0x10ff
	s_cselect_b64 s[8:9], -1, 0
	s_and_b64 vcc, exec, s[8:9]
	s_cbranch_vccnz .LBB0_313
	v_lshl_add_u32 v2, s22, 1, v39
	s_mov_b32 s0, 0x78787879
	v_mul_hi_i32 v3, v2, s0
	v_lshrrev_b32_e32 v4, 31, v3
	v_ashrrev_i32_e32 v3, 7, v3
	v_add_u32_e32 v6, v3, v4
	v_mul_i32_i24_e32 v3, 0x110, v6
	v_sub_u32_e32 v2, v2, v3
	v_and_b32_e32 v18, 1, v6
	v_lshl_or_b32 v2, v2, 4, v62
	v_add_u32_e32 v4, 0xffffff00, v2
	v_sub_u32_e32 v5, 0x10ff, v2
	v_cmp_eq_u32_e32 vcc, 0, v18
	v_ashrrev_i32_e32 v3, 3, v6
	s_movk_i32 s0, 0x4000
	v_cndmask_b32_e32 v4, v5, v4, vcc
	v_sub_u32_e32 v5, 0xff, v2
	v_lshl_add_u32 v4, v3, 12, v4
	v_lshlrev_b32_e32 v3, 8, v3
	v_cndmask_b32_e32 v5, v5, v2, vcc
	v_add3_u32 v3, v3, v5, s0
	s_movk_i32 s0, 0x100
	v_cmp_gt_i32_e32 vcc, s0, v2
	v_readlane_b32 s0, v255, 48
	v_lshlrev_b32_e32 v6, 6, v6
	v_cndmask_b32_e32 v2, v4, v3, vcc
	v_ashrrev_i32_e32 v3, 31, v2
	v_lshlrev_b64 v[2:3], 9, v[2:3]
	v_readlane_b32 s1, v255, 49
	v_and_b32_e32 v34, 0x180, v6
	v_lshl_add_u64 v[4:5], s[10:11], 0, v[2:3]
	v_lshl_add_u64 v[6:7], s[0:1], 0, v[2:3]
	v_readlane_b32 s0, v255, 50
	v_readlane_b32 s1, v255, 51
	v_lshl_add_u64 v[4:5], v[4:5], 0, v[34:35]
	v_mov_b32_e32 v37, v35
	v_lshl_add_u64 v[8:9], s[0:1], 0, v[2:3]
	v_readlane_b32 s0, v255, 52
	v_readlane_b32 s1, v255, 53
	v_lshl_add_u64 v[6:7], v[6:7], 0, v[34:35]
	v_lshl_add_u64 v[4:5], v[4:5], 0, v[36:37]
	v_lshl_add_u64 v[10:11], s[0:1], 0, v[2:3]
	v_readlane_b32 s0, v255, 54
	v_lshl_add_u64 v[6:7], v[6:7], 0, v[36:37]
	v_lshl_add_u64 v[8:9], v[8:9], 0, v[34:35]
	v_lshl_add_u64 v[10:11], v[10:11], 0, v[34:35]
	v_readlane_b32 s1, v255, 55
	v_lshl_add_u64 v[8:9], v[8:9], 0, v[36:37]
	v_lshl_add_u64 v[10:11], v[10:11], 0, v[36:37]
	global_load_dwordx2 v[4:5], v[4:5], off
	s_nop 0
	global_load_dwordx2 v[12:13], v[6:7], off
	global_load_dwordx2 v[14:15], v[8:9], off
	global_load_dwordx2 v[16:17], v[10:11], off
	v_lshl_add_u64 v[6:7], s[0:1], 0, v[2:3]
	v_lshl_add_u64 v[6:7], v[6:7], 0, v[34:35]
	v_lshl_add_u64 v[6:7], v[6:7], 0, v[36:37]
	global_load_dwordx2 v[20:21], v[6:7], off
	v_mul_u32_u24_e32 v6, 0x440000, v18
	v_lshlrev_b32_e32 v6, 1, v6
	v_mov_b32_e32 v7, v35
	v_lshl_add_u64 v[6:7], s[10:11], 0, v[6:7]
	v_lshl_add_u64 v[2:3], v[6:7], 0, v[2:3]
	v_lshl_add_u64 v[2:3], v[2:3], 0, v[34:35]
	v_lshl_add_u64 v[2:3], v[2:3], 0, v[36:37]
	v_add_co_u32_e32 v2, vcc, 0x2a80000, v2
	s_nop 1
	v_addc_co_u32_e32 v3, vcc, 0, v3, vcc
	global_load_dwordx2 v[24:25], v[2:3], off

.LBB0_1226:
	s_andn2_b64 vcc, exec, s[0:1]
	s_cbranch_vccnz .LBB0_1318
	v_mov_b32_e32 v2, v0
	s_movk_i32 s0, 0x1000
	s_nop 0
	v_readfirstlane_b32 s6, v2
	v_cmp_gt_i32_e32 vcc, s0, v2
	v_ashrrev_i32_e32 v3, 31, v2
	s_and_saveexec_b64 s[0:1], vcc
	s_movk_i32 s7, 0xdff
	s_cbranch_execz .LBB0_1230
	v_readlane_b32 s2, v255, 37
	v_readlane_b32 s3, v255, 38
	v_readlane_b32 s36, v252, 32
	s_lshl_b64 s[2:3], s[2:3], 16
	v_readlane_b32 s38, v252, 34
	v_readlane_b32 s39, v252, 35
	s_add_u32 s2, s38, s2
	s_addc_u32 s3, s39, s3
	s_add_i32 s4, 0, 0x2000
	v_add_u32_e32 v1, 0xfffffe00, v2
	v_lshl_add_u32 v6, v2, 4, s4
	v_lshlrev_b32_e32 v4, 2, v2
	s_mov_b64 s[4:5], 0
	v_readlane_b32 s37, v252, 33
	v_readlane_b32 s40, v252, 36
	v_readlane_b32 s41, v252, 37
	v_readlane_b32 s42, v252, 38
	v_readlane_b32 s43, v252, 39
	v_readlane_b32 s44, v252, 40
	v_readlane_b32 s45, v252, 41
	v_readlane_b32 s46, v252, 42
	v_readlane_b32 s47, v252, 43
	v_readlane_b32 s48, v252, 44
	v_readlane_b32 s49, v252, 45
	v_readlane_b32 s50, v252, 46
	v_readlane_b32 s51, v252, 47
	v_ashrrev_i32_e32 v5, 31, v4
	v_lshl_add_u64 v[96:97], v[4:5], 2, s[2:3]
	s_mov_b64 s[4:5], 0x2000
	global_load_dwordx4 v[64:67], v[96:97], off
	v_lshl_add_u64 v[96:97], v[96:97], 0, s[4:5]
	global_load_dwordx4 v[68:71], v[96:97], off
	v_lshl_add_u64 v[96:97], v[96:97], 0, s[4:5]
	global_load_dwordx4 v[72:75], v[96:97], off
	v_lshl_add_u64 v[96:97], v[96:97], 0, s[4:5]
	global_load_dwordx4 v[76:79], v[96:97], off
	v_lshl_add_u64 v[96:97], v[96:97], 0, s[4:5]
	global_load_dwordx4 v[80:83], v[96:97], off
	v_lshl_add_u64 v[96:97], v[96:97], 0, s[4:5]
	global_load_dwordx4 v[84:87], v[96:97], off
	v_lshl_add_u64 v[96:97], v[96:97], 0, s[4:5]
	global_load_dwordx4 v[88:91], v[96:97], off
	v_lshl_add_u64 v[96:97], v[96:97], 0, s[4:5]
	global_load_dwordx4 v[92:95], v[96:97], off
	s_waitcnt vmcnt(0)
	ds_write_b128 v6, v[64:67]
	ds_write_b128 v6, v[68:71] offset:8192
	ds_write_b128 v6, v[72:75] offset:16384
	ds_write_b128 v6, v[76:79] offset:24576
	ds_write_b128 v6, v[80:83] offset:32768
	ds_write_b128 v6, v[84:87] offset:40960
	ds_write_b128 v6, v[88:91] offset:49152
	ds_write_b128 v6, v[92:95] offset:57344

.LBB0_1418:
	s_ashr_i32 s11, s10, 31
	s_lshl_b64 s[2:3], s[10:11], 11
	v_lshl_add_u64 v[2:3], v[18:19], 0, s[2:3]
	global_load_dwordx2 v[4:5], v[2:3], off
	s_waitcnt lgkmcnt(1)
	global_load_dwordx2 v[8:9], v[2:3], off offset:512
	global_load_dwordx2 v[28:29], v[2:3], off offset:1024
	s_lshr_b32 s2, s11, 20
	global_load_dwordx2 v[2:3], v[2:3], off offset:1536
	s_add_i32 s2, s10, s2
	s_ashr_i32 s2, s2, 12
	s_cmpk_lt_i32 s10, 0x4000
	s_cselect_b32 s2, s2, 4
	s_mul_hi_i32 s3, s2, 0x6000
	s_mulk_i32 s2, 0x6000
	s_add_u32 s2, s1, s2
	s_addc_u32 s3, s8, s3
	s_add_u32 s4, s2, 0x3000
	s_addc_u32 s5, s3, 0
	s_add_u32 s2, s2, 0x4000
	s_addc_u32 s3, s3, 0
	s_lshl_b64 s[6:7], s[10:11], 10
	s_waitcnt vmcnt(1)
	v_lshlrev_b32_e32 v30, 16, v28
	v_and_b32_e32 v31, 0xffff0000, v28
	s_waitcnt vmcnt(0) lgkmcnt(0)
	v_lshlrev_b32_e32 v10, 16, v2
	v_and_b32_e32 v17, 0xffff0000, v2
	v_lshlrev_b32_e32 v12, 16, v3
	v_and_b32_e32 v13, 0xffff0000, v3
	v_lshlrev_b32_e32 v3, 16, v5
	v_lshlrev_b32_e32 v2, 16, v4
	v_and_b32_e32 v5, 0xffff0000, v5
	v_and_b32_e32 v4, 0xffff0000, v4
	v_pk_mul_f32 v[6:7], v[4:5], v[4:5]
	v_mul_f32_e32 v11, v30, v30
	v_pk_fma_f32 v[6:7], v[2:3], v[2:3], v[6:7]
	v_mul_f32_e32 v117, v31, v31
	v_pk_add_f32 v[36:37], v[6:7], v[6:7] op_sel_hi:[0,1]
	v_lshlrev_b32_e32 v7, 16, v9
	v_lshlrev_b32_e32 v6, 16, v8
	v_and_b32_e32 v9, 0xffff0000, v9
	v_and_b32_e32 v8, 0xffff0000, v8
	v_pk_mul_f32 v[32:33], v[8:9], v[8:9]
	v_mov_b32_e32 v116, v10
	v_pk_fma_f32 v[32:33], v[6:7], v[6:7], v[32:33]
	v_pk_add_f32 v[116:117], v[10:11], v[116:117]
	v_pk_add_f32 v[114:115], v[32:33], v[32:33] op_sel_hi:[0,1]
	v_lshlrev_b32_e32 v32, 16, v29
	v_and_b32_e32 v33, 0xffff0000, v29
	v_mul_f32_e32 v28, v32, v32
	v_pk_fma_f32 v[28:29], v[32:33], v[32:33], v[28:29] op_sel_hi:[1,1,0]
	v_mul_f32_e32 v36, v12, v12
	v_mul_f32_e32 v28, v17, v17
	v_mul_f32_e32 v114, v13, v13
	v_mul_f32_e32 v118, v10, v10
	v_mov_b32_e32 v119, v117
	v_pk_add_f32 v[28:29], v[118:119], v[28:29]
	v_pk_add_f32 v[36:37], v[36:37], v[114:115]
	global_load_dwordx4 v[114:117], v[22:23], off
	global_load_dwordx4 v[118:121], v21, s[4:5]
	global_load_dwordx4 v[122:125], v21, s[2:3]
	global_load_dwordx4 v[128:131], v[22:23], off offset:1024
	global_load_dwordx4 v[132:135], v34, s[4:5]
	global_load_dwordx4 v[136:139], v34, s[2:3]
	global_load_dwordx4 v[140:143], v[22:23], off offset:2048
	global_load_dwordx4 v[144:147], v109, s[4:5]
	global_load_dwordx4 v[148:151], v109, s[2:3]
	global_load_dwordx4 v[152:155], v[22:23], off offset:3072
	global_load_dwordx4 v[156:159], v110, s[4:5]
	global_load_dwordx4 v[160:163], v110, s[2:3]
	v_pk_add_f32 v[28:29], v[28:29], v[36:37]
	v_mov_b32_e32 v36, v3
	v_add_f32_e32 v11, v28, v29
	s_nop 1
	v_mov_b32_dpp v27, v11 quad_perm:[1,0,3,2] row_mask:0xf bank_mask:0xf
	v_mov_b32_e32 v3, v4
	v_mov_b32_e32 v37, v5
	v_mov_b32_e32 v126, v7
	v_mov_b32_e32 v127, v9
	s_waitcnt lgkmcnt(0)
	v_add_f32_e32 v11, v11, v27
	s_nop 1
	v_mov_b32_dpp v27, v11 quad_perm:[2,3,0,1] row_mask:0xf bank_mask:0xf
	v_mov_b32_e32 v7, v8
	s_waitcnt lgkmcnt(0)
	v_add_f32_e32 v11, v11, v27
	s_nop 1
	v_mov_b32_dpp v27, v11 row_half_mirror row_mask:0xf bank_mask:0xf
	s_waitcnt lgkmcnt(0)
	v_add_f32_e32 v11, v11, v27
	s_nop 1
	v_mov_b32_dpp v27, v11 row_mirror row_mask:0xf bank_mask:0xf
	s_waitcnt lgkmcnt(0)
	v_add_f32_e32 v11, v11, v27
	v_mov_b32_e32 v27, v11
	s_nop 1
	v_permlane16_swap_b32_e32 v27, v11
	s_waitcnt lgkmcnt(0)
	v_add_f32_e32 v11, v11, v27
	v_mov_b32_e32 v27, v11
	s_nop 1
	v_permlane32_swap_b32_e32 v27, v11
	s_waitcnt lgkmcnt(0)
	v_add_f32_e32 v11, v11, v27
	v_fmamk_f32 v11, v11, 0x3a800000, v165
	v_rsq_f32_e32 v28, v11
	s_nop 0
	v_pk_mul_f32 v[2:3], v[2:3], v[28:29] op_sel_hi:[1,0]
	v_pk_mul_f32 v[36:37], v[36:37], v[28:29] op_sel_hi:[1,0]
	s_waitcnt vmcnt(11)
	v_pk_mul_f32 v[2:3], v[114:115], v[2:3]
	v_pk_mul_f32 v[4:5], v[116:117], v[36:37]
	s_waitcnt vmcnt(9)
	v_pk_add_f32 v[114:115], v[122:123], 1.0 op_sel_hi:[1,0]
	v_pk_add_f32 v[36:37], v[124:125], 1.0 op_sel_hi:[1,0]
	v_pk_fma_f32 v[2:3], v[114:115], v[2:3], v[118:119]
	v_mov_b32_e32 v114, v35
	v_med3_f32 v11, v2, s13, v200
	v_med3_f32 v27, v3, s13, v200
	v_cvt_pk_fp8_f32 v114, v11, v27
	v_pk_fma_f32 v[4:5], v[36:37], v[4:5], v[120:121]
	s_nop 0
	v_med3_f32 v29, v4, s13, v200
	v_med3_f32 v36, v5, s13, v200
	v_cvt_pk_fp8_f32 v114, v29, v36 op_sel:[0,0,1]
	v_lshl_add_u64 v[36:37], v[24:25], 0, s[6:7]
	v_pk_mul_f32 v[126:127], v[126:127], v[28:29] op_sel_hi:[1,0]
	v_pk_mul_f32 v[6:7], v[6:7], v[28:29] op_sel_hi:[1,0]
	global_store_dword v[36:37], v114, off
	s_waitcnt vmcnt(7)
	v_mov_b64_e32 v[114:115], v[128:129]
	v_mov_b64_e32 v[116:117], v[130:131]
	v_mov_b64_e32 v[118:119], v[132:133]
	v_mov_b64_e32 v[120:121], v[134:135]
	v_mov_b64_e32 v[122:123], v[136:137]
	v_mov_b64_e32 v[124:125], v[138:139]
	s_add_i32 s6, s10, 1
	s_ashr_i32 s7, s6, 31
	s_nop 0
	v_pk_mul_f32 v[6:7], v[114:115], v[6:7]
	v_pk_mul_f32 v[8:9], v[116:117], v[126:127]
	s_nop 0
	v_pk_add_f32 v[116:117], v[122:123], 1.0 op_sel_hi:[1,0]
	v_pk_add_f32 v[114:115], v[124:125], 1.0 op_sel_hi:[1,0]
	v_pk_fma_f32 v[6:7], v[116:117], v[6:7], v[118:119]
	v_pk_fma_f32 v[8:9], v[114:115], v[8:9], v[120:121]
	v_med3_f32 v11, v6, s13, v200
	v_med3_f32 v27, v7, s13, v200
	v_mov_b32_e32 v115, v35
	v_cvt_pk_fp8_f32 v115, v11, v27
	v_med3_f32 v29, v8, s13, v200
	v_med3_f32 v114, v9, s13, v200
	v_pk_mul_f32 v[32:33], v[32:33], v[28:29] op_sel_hi:[1,0]
	v_cvt_pk_fp8_f32 v115, v29, v114 op_sel:[0,0,1]
	v_pk_mul_f32 v[30:31], v[30:31], v[28:29] op_sel_hi:[1,0]
	global_store_dword v[36:37], v115, off offset:256
	s_waitcnt vmcnt(5)
	v_mov_b64_e32 v[114:115], v[140:141]
	v_mov_b64_e32 v[116:117], v[142:143]
	v_mov_b64_e32 v[118:119], v[144:145]
	v_mov_b64_e32 v[120:121], v[146:147]
	v_mov_b64_e32 v[122:123], v[148:149]
	v_mov_b64_e32 v[124:125], v[150:151]
	s_nop 0
	v_pk_mul_f32 v[30:31], v[30:31], v[114:115]
	v_pk_mul_f32 v[32:33], v[32:33], v[116:117]
	s_nop 0
	v_pk_add_f32 v[116:117], v[122:123], 1.0 op_sel_hi:[1,0]
	v_pk_add_f32 v[114:115], v[124:125], 1.0 op_sel_hi:[1,0]
	v_pk_fma_f32 v[30:31], v[30:31], v[116:117], v[118:119]
	v_pk_fma_f32 v[32:33], v[32:33], v[114:115], v[120:121]
	v_med3_f32 v11, v30, s13, v200
	v_med3_f32 v27, v31, s13, v200
	v_mov_b32_e32 v115, v35
	v_cvt_pk_fp8_f32 v115, v11, v27
	v_med3_f32 v29, v32, s13, v200
	v_med3_f32 v114, v33, s13, v200
	v_mov_b32_e32 v11, v17
	v_cvt_pk_fp8_f32 v115, v29, v114 op_sel:[0,0,1]
	v_pk_mul_f32 v[10:11], v[10:11], v[28:29] op_sel_hi:[1,0]
	v_pk_mul_f32 v[12:13], v[12:13], v[28:29] op_sel_hi:[1,0]
	global_store_dword v[36:37], v115, off offset:512
	s_waitcnt vmcnt(3)
	v_mov_b64_e32 v[114:115], v[152:153]
	v_mov_b64_e32 v[116:117], v[154:155]
	v_mov_b64_e32 v[118:119], v[156:157]
	v_mov_b64_e32 v[120:121], v[158:159]
	v_mov_b64_e32 v[122:123], v[160:161]
	v_mov_b64_e32 v[124:125], v[162:163]
	s_lshl_b64 s[2:3], s[6:7], 11
	s_nop 0
	v_pk_mul_f32 v[10:11], v[10:11], v[114:115]
	v_pk_mul_f32 v[12:13], v[12:13], v[116:117]
	s_nop 0
	v_pk_add_f32 v[114:115], v[122:123], 1.0 op_sel_hi:[1,0]
	v_pk_add_f32 v[28:29], v[124:125], 1.0 op_sel_hi:[1,0]
	v_pk_fma_f32 v[10:11], v[10:11], v[114:115], v[118:119]
	v_mov_b32_e32 v114, v35
	v_med3_f32 v17, v10, s13, v200
	v_med3_f32 v27, v11, s13, v200
	v_cvt_pk_fp8_f32 v114, v17, v27
	v_pk_fma_f32 v[12:13], v[12:13], v[28:29], v[120:121]
	v_add_u32_e32 v17, s9, v20
	v_med3_f32 v28, v12, s13, v200
	v_med3_f32 v29, v13, s13, v200
	v_cvt_pk_fp8_f32 v114, v28, v29 op_sel:[0,0,1]
	global_store_dword v[36:37], v114, off offset:768
	ds_write_b128 v17, v[2:5]
	ds_write_b128 v17, v[6:9] offset:1024
	ds_write_b128 v17, v[30:33] offset:2048
	ds_write_b128 v17, v[10:13] offset:3072
	v_lshl_add_u64 v[2:3], v[18:19], 0, s[2:3]
	global_load_dwordx2 v[4:5], v[2:3], off
	global_load_dwordx2 v[8:9], v[2:3], off offset:512
	global_load_dwordx2 v[12:13], v[2:3], off offset:1024
	s_lshr_b32 s2, s7, 20
	global_load_dwordx2 v[2:3], v[2:3], off offset:1536
	s_add_i32 s2, s6, s2
	s_ashr_i32 s2, s2, 12
	s_cmpk_lt_i32 s6, 0x4000
	s_cselect_b32 s2, s2, 4
	s_mul_hi_i32 s3, s2, 0x6000
	s_mulk_i32 s2, 0x6000
	s_add_u32 s2, s1, s2
	s_addc_u32 s3, s8, s3
	s_add_u32 s4, s2, 0x3000
	s_addc_u32 s5, s3, 0
	s_add_u32 s2, s2, 0x4000
	s_addc_u32 s3, s3, 0
	s_lshl_b64 s[6:7], s[6:7], 10
	s_waitcnt vmcnt(1)
	v_lshlrev_b32_e32 v10, 16, v12
	v_and_b32_e32 v11, 0xffff0000, v12
	s_waitcnt vmcnt(0)
	v_lshlrev_b32_e32 v28, 16, v2
	v_and_b32_e32 v17, 0xffff0000, v2
	v_lshlrev_b32_e32 v30, 16, v3
	v_and_b32_e32 v31, 0xffff0000, v3
	v_lshlrev_b32_e32 v3, 16, v5
	v_lshlrev_b32_e32 v2, 16, v4
	v_and_b32_e32 v5, 0xffff0000, v5
	v_and_b32_e32 v4, 0xffff0000, v4
	v_pk_mul_f32 v[6:7], v[4:5], v[4:5]
	v_lshlrev_b32_e32 v12, 16, v13
	v_pk_fma_f32 v[6:7], v[2:3], v[2:3], v[6:7]
	v_mul_f32_e32 v29, v10, v10
	v_pk_add_f32 v[32:33], v[6:7], v[6:7] op_sel_hi:[0,1]
	v_lshlrev_b32_e32 v7, 16, v9
	v_lshlrev_b32_e32 v6, 16, v8
	v_and_b32_e32 v9, 0xffff0000, v9
	v_and_b32_e32 v8, 0xffff0000, v8
	v_pk_mul_f32 v[36:37], v[8:9], v[8:9]
	v_mul_f32_e32 v115, v11, v11
	v_pk_fma_f32 v[36:37], v[6:7], v[6:7], v[36:37]
	v_and_b32_e32 v13, 0xffff0000, v13
	v_mul_f32_e32 v32, v12, v12
	v_mov_b32_e32 v114, v28
	v_pk_add_f32 v[36:37], v[36:37], v[36:37] op_sel_hi:[0,1]
	v_pk_fma_f32 v[116:117], v[12:13], v[12:13], v[32:33] op_sel_hi:[1,1,0]
	v_pk_add_f32 v[114:115], v[28:29], v[114:115]
	v_mul_f32_e32 v116, v17, v17
	v_mul_f32_e32 v32, v30, v30
	v_mul_f32_e32 v36, v31, v31
	v_mul_f32_e32 v118, v28, v28
	v_mov_b32_e32 v119, v115
	v_pk_add_f32 v[114:115], v[118:119], v[116:117]
	v_pk_add_f32 v[32:33], v[32:33], v[36:37]
	v_mov_b32_e32 v36, v3
	v_pk_add_f32 v[32:33], v[114:115], v[32:33]
	global_load_dwordx4 v[114:117], v[22:23], off
	global_load_dwordx4 v[118:121], v21, s[4:5]
	global_load_dwordx4 v[122:125], v21, s[2:3]
	global_load_dwordx4 v[128:131], v[22:23], off offset:1024
	global_load_dwordx4 v[132:135], v34, s[4:5]
	global_load_dwordx4 v[136:139], v34, s[2:3]
	global_load_dwordx4 v[140:143], v[22:23], off offset:2048
	global_load_dwordx4 v[144:147], v109, s[4:5]
	global_load_dwordx4 v[148:151], v109, s[2:3]
	global_load_dwordx4 v[152:155], v[22:23], off offset:3072
	global_load_dwordx4 v[156:159], v110, s[4:5]
	global_load_dwordx4 v[160:163], v110, s[2:3]
	v_add_f32_e32 v27, v32, v33
	s_nop 1
	v_mov_b32_dpp v29, v27 quad_perm:[1,0,3,2] row_mask:0xf bank_mask:0xf
	v_mov_b32_e32 v3, v4
	v_mov_b32_e32 v37, v5
	v_mov_b32_e32 v126, v7
	v_mov_b32_e32 v127, v9
	s_waitcnt lgkmcnt(0)
	v_add_f32_e32 v27, v27, v29
	s_nop 1
	v_mov_b32_dpp v29, v27 quad_perm:[2,3,0,1] row_mask:0xf bank_mask:0xf
	v_mov_b32_e32 v7, v8
	s_waitcnt lgkmcnt(0)
	v_add_f32_e32 v27, v27, v29
	s_nop 1
	v_mov_b32_dpp v29, v27 row_half_mirror row_mask:0xf bank_mask:0xf
	s_waitcnt lgkmcnt(0)
	v_add_f32_e32 v27, v27, v29
	s_nop 1
	v_mov_b32_dpp v29, v27 row_mirror row_mask:0xf bank_mask:0xf
	s_waitcnt lgkmcnt(0)
	v_add_f32_e32 v27, v27, v29
	v_mov_b32_e32 v29, v27
	s_nop 1
	v_permlane16_swap_b32_e32 v29, v27
	s_waitcnt lgkmcnt(0)
	v_add_f32_e32 v27, v27, v29
	v_mov_b32_e32 v29, v27
	s_nop 1
	v_permlane32_swap_b32_e32 v29, v27
	s_waitcnt lgkmcnt(0)
	v_add_f32_e32 v27, v27, v29
	v_fmamk_f32 v27, v27, 0x3a800000, v165
	v_rsq_f32_e32 v32, v27
	s_nop 0
	v_pk_mul_f32 v[2:3], v[2:3], v[32:33] op_sel_hi:[1,0]
	v_pk_mul_f32 v[36:37], v[36:37], v[32:33] op_sel_hi:[1,0]
	s_waitcnt vmcnt(11)
	v_pk_mul_f32 v[2:3], v[114:115], v[2:3]
	v_pk_mul_f32 v[4:5], v[116:117], v[36:37]
	s_waitcnt vmcnt(9)
	v_pk_add_f32 v[114:115], v[122:123], 1.0 op_sel_hi:[1,0]
	v_pk_add_f32 v[36:37], v[124:125], 1.0 op_sel_hi:[1,0]
	v_pk_fma_f32 v[2:3], v[114:115], v[2:3], v[118:119]
	v_mov_b32_e32 v114, v35
	v_med3_f32 v27, v2, s13, v200
	v_med3_f32 v29, v3, s13, v200
	v_cvt_pk_fp8_f32 v114, v27, v29
	v_pk_fma_f32 v[4:5], v[36:37], v[4:5], v[120:121]
	s_nop 0
	v_med3_f32 v33, v4, s13, v200
	v_med3_f32 v36, v5, s13, v200
	v_cvt_pk_fp8_f32 v114, v33, v36 op_sel:[0,0,1]
	v_lshl_add_u64 v[36:37], v[24:25], 0, s[6:7]
	v_pk_mul_f32 v[126:127], v[126:127], v[32:33] op_sel_hi:[1,0]
	v_pk_mul_f32 v[6:7], v[6:7], v[32:33] op_sel_hi:[1,0]
	global_store_dword v[36:37], v114, off
	s_waitcnt vmcnt(7)
	v_mov_b64_e32 v[114:115], v[128:129]
	v_mov_b64_e32 v[116:117], v[130:131]
	v_mov_b64_e32 v[118:119], v[132:133]
	v_mov_b64_e32 v[120:121], v[134:135]
	v_mov_b64_e32 v[122:123], v[136:137]
	v_mov_b64_e32 v[124:125], v[138:139]
	s_nop 0
	v_pk_mul_f32 v[6:7], v[114:115], v[6:7]
	v_pk_mul_f32 v[8:9], v[116:117], v[126:127]
	s_nop 0
	v_pk_add_f32 v[116:117], v[122:123], 1.0 op_sel_hi:[1,0]
	v_pk_add_f32 v[114:115], v[124:125], 1.0 op_sel_hi:[1,0]
	v_pk_fma_f32 v[6:7], v[116:117], v[6:7], v[118:119]
	v_pk_fma_f32 v[8:9], v[114:115], v[8:9], v[120:121]
	v_med3_f32 v27, v6, s13, v200
	v_med3_f32 v29, v7, s13, v200
	v_mov_b32_e32 v115, v35
	v_cvt_pk_fp8_f32 v115, v27, v29
	v_med3_f32 v33, v8, s13, v200
	v_med3_f32 v114, v9, s13, v200
	v_pk_mul_f32 v[12:13], v[12:13], v[32:33] op_sel_hi:[1,0]
	v_cvt_pk_fp8_f32 v115, v33, v114 op_sel:[0,0,1]
	v_pk_mul_f32 v[10:11], v[10:11], v[32:33] op_sel_hi:[1,0]
	global_store_dword v[36:37], v115, off offset:256
	s_waitcnt vmcnt(5)
	v_mov_b64_e32 v[114:115], v[140:141]
	v_mov_b64_e32 v[116:117], v[142:143]
	v_mov_b64_e32 v[118:119], v[144:145]
	v_mov_b64_e32 v[120:121], v[146:147]
	v_mov_b64_e32 v[122:123], v[148:149]
	v_mov_b64_e32 v[124:125], v[150:151]
	s_nop 0
	v_pk_mul_f32 v[10:11], v[10:11], v[114:115]
	v_pk_mul_f32 v[12:13], v[12:13], v[116:117]
	s_nop 0
	v_pk_add_f32 v[116:117], v[122:123], 1.0 op_sel_hi:[1,0]
	v_pk_add_f32 v[114:115], v[124:125], 1.0 op_sel_hi:[1,0]
	v_pk_fma_f32 v[10:11], v[10:11], v[116:117], v[118:119]
	v_pk_fma_f32 v[12:13], v[12:13], v[114:115], v[120:121]
	v_med3_f32 v27, v10, s13, v200
	v_med3_f32 v29, v11, s13, v200
	v_mov_b32_e32 v115, v35
	v_cvt_pk_fp8_f32 v115, v27, v29
	v_med3_f32 v33, v12, s13, v200
	v_med3_f32 v114, v13, s13, v200
	v_mov_b32_e32 v29, v17
	v_cvt_pk_fp8_f32 v115, v33, v114 op_sel:[0,0,1]
	v_pk_mul_f32 v[28:29], v[28:29], v[32:33] op_sel_hi:[1,0]
	v_pk_mul_f32 v[30:31], v[30:31], v[32:33] op_sel_hi:[1,0]
	global_store_dword v[36:37], v115, off offset:512
	s_waitcnt vmcnt(3)
	v_mov_b64_e32 v[114:115], v[152:153]
	v_mov_b64_e32 v[116:117], v[154:155]
	v_mov_b64_e32 v[118:119], v[156:157]
	v_mov_b64_e32 v[120:121], v[158:159]
	v_mov_b64_e32 v[122:123], v[160:161]
	v_mov_b64_e32 v[124:125], v[162:163]
	s_nop 0
	v_pk_mul_f32 v[28:29], v[28:29], v[114:115]
	v_pk_mul_f32 v[30:31], v[30:31], v[116:117]
	s_nop 0
	v_pk_add_f32 v[114:115], v[122:123], 1.0 op_sel_hi:[1,0]
	v_pk_add_f32 v[32:33], v[124:125], 1.0 op_sel_hi:[1,0]
	v_pk_fma_f32 v[28:29], v[28:29], v[114:115], v[118:119]
	v_mov_b32_e32 v114, v35
	v_med3_f32 v17, v28, s13, v200
	v_med3_f32 v27, v29, s13, v200
	v_cvt_pk_fp8_f32 v114, v17, v27
	v_pk_fma_f32 v[30:31], v[30:31], v[32:33], v[120:121]
	v_add_u32_e32 v17, s14, v20
	v_med3_f32 v32, v30, s13, v200
	v_med3_f32 v33, v31, s13, v200
	v_cvt_pk_fp8_f32 v114, v32, v33 op_sel:[0,0,1]
	global_store_dword v[36:37], v114, off offset:768
	ds_write_b128 v17, v[2:5]
	ds_write_b128 v17, v[6:9] offset:1024
	ds_write_b128 v17, v[10:13] offset:2048
	ds_write_b128 v17, v[28:31] offset:3072
	s_waitcnt lgkmcnt(0)
	s_barrier
	ds_read2_b32 v[10:11], v111 offset1:4
	ds_read2_b32 v[12:13], v111 offset0:8 offset1:12
	s_waitcnt lgkmcnt(1)
	v_mfma_f32_16x16x4_f32 v[2:5], v10, v39, 0
	v_mfma_f32_16x16x4_f32 v[6:9], v10, v46, 0
	v_mfma_f32_16x16x4_f32 v[2:5], v11, v40, v[2:5]
	v_mfma_f32_16x16x4_f32 v[6:9], v11, v45, v[6:9]
	ds_read2_b32 v[10:11], v111 offset0:16 offset1:20
	s_waitcnt lgkmcnt(1)
	v_mfma_f32_16x16x4_f32 v[2:5], v12, v41, v[2:5]
	v_mfma_f32_16x16x4_f32 v[6:9], v12, v44, v[6:9]
	v_mfma_f32_16x16x4_f32 v[2:5], v13, v42, v[2:5]
	v_mfma_f32_16x16x4_f32 v[6:9], v13, v43, v[6:9]
	s_waitcnt lgkmcnt(0)
	v_mfma_f32_16x16x4_f32 v[2:5], v10, v47, v[2:5]
	v_mfma_f32_16x16x4_f32 v[6:9], v10, v54, v[6:9]
	v_mfma_f32_16x16x4_f32 v[2:5], v11, v48, v[2:5]
	v_mfma_f32_16x16x4_f32 v[6:9], v11, v53, v[6:9]
	ds_read2_b32 v[10:11], v111 offset0:24 offset1:28
	s_waitcnt lgkmcnt(0)
	v_mfma_f32_16x16x4_f32 v[2:5], v10, v49, v[2:5]
	v_mfma_f32_16x16x4_f32 v[6:9], v10, v52, v[6:9]
	v_mfma_f32_16x16x4_f32 v[2:5], v11, v50, v[2:5]
	v_mfma_f32_16x16x4_f32 v[6:9], v11, v51, v[6:9]
	ds_read2_b32 v[10:11], v111 offset0:32 offset1:36
	s_waitcnt lgkmcnt(0)
	v_mfma_f32_16x16x4_f32 v[2:5], v10, v55, v[2:5]
	v_mfma_f32_16x16x4_f32 v[6:9], v10, v62, v[6:9]
	v_mfma_f32_16x16x4_f32 v[2:5], v11, v56, v[2:5]
	v_mfma_f32_16x16x4_f32 v[6:9], v11, v61, v[6:9]
	ds_read2_b32 v[10:11], v111 offset0:40 offset1:44
	s_waitcnt lgkmcnt(0)
	v_mfma_f32_16x16x4_f32 v[2:5], v10, v57, v[2:5]
	v_mfma_f32_16x16x4_f32 v[6:9], v10, v60, v[6:9]
	v_mfma_f32_16x16x4_f32 v[2:5], v11, v58, v[2:5]
	v_mfma_f32_16x16x4_f32 v[6:9], v11, v59, v[6:9]
	ds_read2_b32 v[10:11], v111 offset0:48 offset1:52
	s_waitcnt lgkmcnt(0)
	v_mfma_f32_16x16x4_f32 v[2:5], v10, v63, v[2:5]
	v_mfma_f32_16x16x4_f32 v[6:9], v10, v70, v[6:9]
	v_mfma_f32_16x16x4_f32 v[2:5], v11, v64, v[2:5]
	v_mfma_f32_16x16x4_f32 v[6:9], v11, v69, v[6:9]
	ds_read2_b32 v[10:11], v111 offset0:56 offset1:60
	s_waitcnt lgkmcnt(0)
	v_mfma_f32_16x16x4_f32 v[2:5], v10, v65, v[2:5]
	v_mfma_f32_16x16x4_f32 v[6:9], v10, v68, v[6:9]
	v_mfma_f32_16x16x4_f32 v[2:5], v11, v66, v[2:5]
	v_mfma_f32_16x16x4_f32 v[6:9], v11, v67, v[6:9]
	ds_read2_b32 v[10:11], v111 offset0:64 offset1:68
	s_waitcnt lgkmcnt(0)
	v_mfma_f32_16x16x4_f32 v[2:5], v10, v71, v[2:5]
	v_mfma_f32_16x16x4_f32 v[6:9], v10, v78, v[6:9]
	v_mfma_f32_16x16x4_f32 v[2:5], v11, v72, v[2:5]
	v_mfma_f32_16x16x4_f32 v[6:9], v11, v77, v[6:9]
	ds_read2_b32 v[10:11], v111 offset0:72 offset1:76
	s_waitcnt lgkmcnt(0)
	v_mfma_f32_16x16x4_f32 v[2:5], v10, v73, v[2:5]
	v_mfma_f32_16x16x4_f32 v[6:9], v10, v76, v[6:9]
	v_mfma_f32_16x16x4_f32 v[2:5], v11, v74, v[2:5]
	v_mfma_f32_16x16x4_f32 v[6:9], v11, v75, v[6:9]
	ds_read2_b32 v[10:11], v111 offset0:80 offset1:84
	s_waitcnt lgkmcnt(0)
	v_mfma_f32_16x16x4_f32 v[2:5], v10, v79, v[2:5]
	v_mfma_f32_16x16x4_f32 v[6:9], v10, v86, v[6:9]
	v_mfma_f32_16x16x4_f32 v[2:5], v11, v80, v[2:5]
	v_mfma_f32_16x16x4_f32 v[6:9], v11, v85, v[6:9]
	ds_read2_b32 v[10:11], v111 offset0:88 offset1:92
	s_waitcnt lgkmcnt(0)
	v_mfma_f32_16x16x4_f32 v[2:5], v10, v81, v[2:5]
	v_mfma_f32_16x16x4_f32 v[6:9], v10, v84, v[6:9]
	v_mfma_f32_16x16x4_f32 v[2:5], v11, v82, v[2:5]
	v_mfma_f32_16x16x4_f32 v[6:9], v11, v83, v[6:9]
	ds_read2_b32 v[10:11], v111 offset0:96 offset1:100
	s_waitcnt lgkmcnt(0)
	v_mfma_f32_16x16x4_f32 v[2:5], v10, v87, v[2:5]
	v_mfma_f32_16x16x4_f32 v[6:9], v10, v94, v[6:9]
	v_mfma_f32_16x16x4_f32 v[2:5], v11, v88, v[2:5]
	v_mfma_f32_16x16x4_f32 v[6:9], v11, v93, v[6:9]
	ds_read2_b32 v[10:11], v111 offset0:104 offset1:108
	s_waitcnt lgkmcnt(0)
	v_mfma_f32_16x16x4_f32 v[2:5], v10, v89, v[2:5]
	v_mfma_f32_16x16x4_f32 v[6:9], v10, v92, v[6:9]
	v_mfma_f32_16x16x4_f32 v[2:5], v11, v90, v[2:5]
	v_mfma_f32_16x16x4_f32 v[6:9], v11, v91, v[6:9]
	ds_read2_b32 v[10:11], v111 offset0:112 offset1:116
	s_waitcnt lgkmcnt(0)
	v_mfma_f32_16x16x4_f32 v[2:5], v10, v95, v[2:5]
	v_mfma_f32_16x16x4_f32 v[6:9], v10, v102, v[6:9]
	v_mfma_f32_16x16x4_f32 v[2:5], v11, v96, v[2:5]
	v_mfma_f32_16x16x4_f32 v[6:9], v11, v101, v[6:9]
	ds_read2_b32 v[10:11], v111 offset0:120 offset1:124
	s_waitcnt lgkmcnt(0)
	v_mfma_f32_16x16x4_f32 v[2:5], v10, v97, v[2:5]
	v_mfma_f32_16x16x4_f32 v[6:9], v10, v100, v[6:9]
	v_mfma_f32_16x16x4_f32 v[2:5], v11, v98, v[2:5]
	v_mfma_f32_16x16x4_f32 v[6:9], v11, v99, v[6:9]
	s_nop 9
	ds_write2_b32 v112, v2, v6 offset1:16
	ds_write2_b32 v112, v3, v7 offset0:33 offset1:49
	ds_write2_b32 v112, v4, v8 offset0:66 offset1:82
	ds_write2_b32 v112, v5, v9 offset0:99 offset1:115
	s_waitcnt lgkmcnt(0)
	s_barrier
	ds_read_b32 v2, v113
	ds_read_b32 v3, v113 offset:2112
	s_waitcnt lgkmcnt(1)
	v_add_f32_e32 v2, v38, v2
	s_waitcnt lgkmcnt(0)
	v_add_f32_e32 v2, v2, v3
	ds_read_b32 v3, v113 offset:4224
	s_waitcnt lgkmcnt(0)
	v_add_f32_e32 v2, v2, v3
	ds_read_b32 v3, v113 offset:6336
	s_waitcnt lgkmcnt(0)
	v_add_f32_e32 v2, v2, v3
	ds_read_b32 v3, v113 offset:8448
	s_waitcnt lgkmcnt(0)
	v_add_f32_e32 v2, v2, v3
	ds_read_b32 v3, v113 offset:10560
	s_waitcnt lgkmcnt(0)
	v_add_f32_e32 v2, v2, v3
	ds_read_b32 v3, v113 offset:12672
	s_waitcnt lgkmcnt(0)
	v_add_f32_e32 v2, v2, v3
	ds_read_b32 v3, v113 offset:14784
	s_waitcnt lgkmcnt(0)
	v_add_f32_e32 v2, v2, v3
	v_not_b32_e32 v3, v2
	v_or_b32_e32 v4, 0x80000000, v2
	v_cmp_gt_i32_e64 s[2:3], 0, v2
	s_nop 1
	v_mov_b32_dpp v2, v16 quad_perm:[1,0,3,2] row_mask:0xf bank_mask:0xf
	s_nop 0
	v_cndmask_b32_e64 v17, v4, v3, s[2:3]
	s_nop 1
	v_mov_b32_dpp v3, v17 quad_perm:[1,0,3,2] row_mask:0xf bank_mask:0xf
	s_waitcnt lgkmcnt(0)
	v_cmp_gt_u64_e64 s[2:3], v[2:3], v[16:17]
	s_nop 1
	v_cndmask_b32_e64 v3, v17, v3, s[2:3]
	v_cndmask_b32_e64 v2, v16, v2, s[2:3]
	s_nop 1
	v_mov_b32_dpp v4, v2 quad_perm:[2,3,0,1] row_mask:0xf bank_mask:0xf
	s_nop 1
	v_mov_b32_dpp v5, v3 quad_perm:[2,3,0,1] row_mask:0xf bank_mask:0xf
	s_waitcnt lgkmcnt(0)
	v_cmp_gt_u64_e64 s[2:3], v[4:5], v[2:3]
	s_nop 1
	v_cndmask_b32_e64 v3, v3, v5, s[2:3]
	v_cndmask_b32_e64 v2, v2, v4, s[2:3]
	s_nop 1
	v_mov_b32_dpp v4, v2 row_half_mirror row_mask:0xf bank_mask:0xf
	s_nop 1
	v_mov_b32_dpp v5, v3 row_half_mirror row_mask:0xf bank_mask:0xf
	s_waitcnt lgkmcnt(0)
	v_cmp_gt_u64_e64 s[2:3], v[4:5], v[2:3]
	s_nop 1
	v_cndmask_b32_e64 v3, v3, v5, s[2:3]
	v_cndmask_b32_e64 v2, v2, v4, s[2:3]
	s_nop 1
	v_mov_b32_dpp v4, v2 row_mirror row_mask:0xf bank_mask:0xf
	s_nop 1
	v_mov_b32_dpp v5, v3 row_mirror row_mask:0xf bank_mask:0xf
	s_waitcnt lgkmcnt(0)
	v_cmp_gt_u64_e64 s[2:3], v[4:5], v[2:3]
	s_nop 1
	v_cndmask_b32_e64 v3, v3, v5, s[2:3]
	v_cndmask_b32_e64 v2, v2, v4, s[2:3]
	ds_bpermute_b32 v4, v107, v2
	ds_bpermute_b32 v5, v107, v3
	s_waitcnt lgkmcnt(0)
	v_cmp_gt_u64_e64 s[2:3], v[4:5], v[2:3]
	s_nop 1
	v_cndmask_b32_e64 v2, v2, v4, s[2:3]
	v_sub_u32_e32 v30, 31, v2
	v_cmp_ne_u32_e64 s[4:5], v30, v15
	s_nop 1
	v_cndmask_b32_e64 v11, 0, v17, s[4:5]
	v_cndmask_b32_e64 v10, 0, v16, s[4:5]
	s_nop 1
	v_mov_b32_dpp v6, v10 quad_perm:[1,0,3,2] row_mask:0xf bank_mask:0xf
	s_nop 1
	v_mov_b32_dpp v7, v11 quad_perm:[1,0,3,2] row_mask:0xf bank_mask:0xf
	s_waitcnt lgkmcnt(0)
	v_cmp_gt_u64_e64 s[4:5], v[6:7], v[10:11]
	s_nop 1
	v_cndmask_b32_e64 v7, v11, v7, s[4:5]
	v_cndmask_b32_e64 v6, v10, v6, s[4:5]
	s_nop 1
	v_mov_b32_dpp v8, v6 quad_perm:[2,3,0,1] row_mask:0xf bank_mask:0xf
	s_nop 1
	v_mov_b32_dpp v9, v7 quad_perm:[2,3,0,1] row_mask:0xf bank_mask:0xf
	s_waitcnt lgkmcnt(0)
	v_cmp_gt_u64_e64 s[4:5], v[8:9], v[6:7]
	s_nop 1
	v_cndmask_b32_e64 v7, v7, v9, s[4:5]
	v_cndmask_b32_e64 v6, v6, v8, s[4:5]
	s_nop 1
	v_mov_b32_dpp v8, v6 row_half_mirror row_mask:0xf bank_mask:0xf
	s_nop 1
	v_mov_b32_dpp v9, v7 row_half_mirror row_mask:0xf bank_mask:0xf
	s_waitcnt lgkmcnt(0)
	v_cmp_gt_u64_e64 s[4:5], v[8:9], v[6:7]
	s_nop 1
	v_cndmask_b32_e64 v7, v7, v9, s[4:5]
	v_cndmask_b32_e64 v6, v6, v8, s[4:5]
	s_nop 1
	v_mov_b32_dpp v8, v6 row_mirror row_mask:0xf bank_mask:0xf
	s_nop 1
	v_mov_b32_dpp v9, v7 row_mirror row_mask:0xf bank_mask:0xf
	s_waitcnt lgkmcnt(0)
	v_cmp_gt_u64_e64 s[4:5], v[8:9], v[6:7]
	s_nop 1
	v_cndmask_b32_e64 v7, v7, v9, s[4:5]
	v_cndmask_b32_e64 v6, v6, v8, s[4:5]
	ds_bpermute_b32 v8, v107, v6
	ds_bpermute_b32 v9, v107, v7
	s_waitcnt lgkmcnt(0)
	v_cmp_gt_u64_e64 s[4:5], v[8:9], v[6:7]
	s_nop 1
	v_cndmask_b32_e64 v4, v6, v8, s[4:5]
	v_sub_u32_e32 v17, 31, v4
	v_cmp_ne_u32_e64 s[6:7], v17, v15
	s_nop 1
	v_cndmask_b32_e64 v29, 0, v11, s[6:7]
	v_cndmask_b32_e64 v28, 0, v10, s[6:7]
	s_nop 1
	v_mov_b32_dpp v10, v28 quad_perm:[1,0,3,2] row_mask:0xf bank_mask:0xf
	s_nop 1
	v_mov_b32_dpp v11, v29 quad_perm:[1,0,3,2] row_mask:0xf bank_mask:0xf
	s_waitcnt lgkmcnt(0)
	v_cmp_gt_u64_e64 s[6:7], v[10:11], v[28:29]
	s_nop 1
	v_cndmask_b32_e64 v11, v29, v11, s[6:7]
	v_cndmask_b32_e64 v10, v28, v10, s[6:7]
	s_nop 1
	v_mov_b32_dpp v12, v10 quad_perm:[2,3,0,1] row_mask:0xf bank_mask:0xf
	s_nop 1
	v_mov_b32_dpp v13, v11 quad_perm:[2,3,0,1] row_mask:0xf bank_mask:0xf
	s_waitcnt lgkmcnt(0)
	v_cmp_gt_u64_e64 s[6:7], v[12:13], v[10:11]
	s_nop 1
	v_cndmask_b32_e64 v11, v11, v13, s[6:7]
	v_cndmask_b32_e64 v10, v10, v12, s[6:7]
	s_nop 1
	v_mov_b32_dpp v12, v10 row_half_mirror row_mask:0xf bank_mask:0xf
	s_nop 1
	v_mov_b32_dpp v13, v11 row_half_mirror row_mask:0xf bank_mask:0xf
	s_waitcnt lgkmcnt(0)
	v_cmp_gt_u64_e64 s[6:7], v[12:13], v[10:11]
	s_nop 1
	v_cndmask_b32_e64 v11, v11, v13, s[6:7]
	v_cndmask_b32_e64 v10, v10, v12, s[6:7]
	s_nop 1
	v_mov_b32_dpp v12, v10 row_mirror row_mask:0xf bank_mask:0xf
	s_nop 1
	v_mov_b32_dpp v13, v11 row_mirror row_mask:0xf bank_mask:0xf
	s_waitcnt lgkmcnt(0)
	v_cmp_gt_u64_e64 s[6:7], v[12:13], v[10:11]
	s_nop 1
	v_cndmask_b32_e64 v11, v11, v13, s[6:7]
	v_cndmask_b32_e64 v10, v10, v12, s[6:7]
	ds_bpermute_b32 v12, v107, v10
	ds_bpermute_b32 v13, v107, v11
	s_waitcnt lgkmcnt(0)
	v_cmp_gt_u64_e64 s[40:41], v[12:13], v[10:11]
	s_nop 1
	v_cndmask_b32_e64 v6, v10, v12, s[40:41]
	v_sub_u32_e32 v12, 31, v6
	v_cmp_ne_u32_e64 s[6:7], v12, v15
	s_nop 1
	v_cndmask_b32_e64 v29, 0, v29, s[6:7]
	v_cndmask_b32_e64 v28, 0, v28, s[6:7]
	s_nop 1
	v_mov_b32_dpp v32, v28 quad_perm:[1,0,3,2] row_mask:0xf bank_mask:0xf
	s_nop 1
	v_mov_b32_dpp v33, v29 quad_perm:[1,0,3,2] row_mask:0xf bank_mask:0xf
	s_waitcnt lgkmcnt(0)
	v_cmp_gt_u64_e64 s[6:7], v[32:33], v[28:29]
	s_nop 1
	v_cndmask_b32_e64 v29, v29, v33, s[6:7]
	v_cndmask_b32_e64 v28, v28, v32, s[6:7]
	s_nop 1
	v_mov_b32_dpp v32, v28 quad_perm:[2,3,0,1] row_mask:0xf bank_mask:0xf
	s_nop 1
	v_mov_b32_dpp v33, v29 quad_perm:[2,3,0,1] row_mask:0xf bank_mask:0xf
	s_waitcnt lgkmcnt(0)
	v_cmp_gt_u64_e64 s[6:7], v[32:33], v[28:29]
	s_nop 1
	v_cndmask_b32_e64 v29, v29, v33, s[6:7]
	v_cndmask_b32_e64 v28, v28, v32, s[6:7]
	s_nop 1
	v_mov_b32_dpp v32, v28 row_half_mirror row_mask:0xf bank_mask:0xf
	s_nop 1
	v_mov_b32_dpp v33, v29 row_half_mirror row_mask:0xf bank_mask:0xf
	s_waitcnt lgkmcnt(0)
	v_cmp_gt_u64_e64 s[6:7], v[32:33], v[28:29]
	s_nop 1
	v_cndmask_b32_e64 v29, v29, v33, s[6:7]
	v_cndmask_b32_e64 v28, v28, v32, s[6:7]
	s_nop 1
	v_mov_b32_dpp v32, v28 row_mirror row_mask:0xf bank_mask:0xf
	s_nop 1
	v_mov_b32_dpp v33, v29 row_mirror row_mask:0xf bank_mask:0xf
	s_waitcnt lgkmcnt(0)
	v_cmp_gt_u64_e64 s[6:7], v[32:33], v[28:29]
	s_nop 1
	v_cndmask_b32_e64 v29, v29, v33, s[6:7]
	v_cndmask_b32_e64 v28, v28, v32, s[6:7]
	ds_bpermute_b32 v8, v107, v28
	ds_bpermute_b32 v10, v107, v29
	s_and_saveexec_b64 s[6:7], s[38:39]
	s_cbranch_execz .LBB0_1417
	v_cndmask_b32_e64 v3, v3, v5, s[2:3]
	v_cndmask_b32_e64 v5, v7, v9, s[4:5]
	s_waitcnt lgkmcnt(0)
	v_mov_b32_e32 v9, v10
	v_cmp_gt_u64_e64 s[2:3], v[8:9], v[28:29]
	v_cndmask_b32_e64 v7, v11, v13, s[40:41]
	v_ashrrev_i32_e32 v27, 31, v26
	v_cndmask_b32_e64 v9, v29, v10, s[2:3]
	v_cndmask_b32_e64 v8, v28, v8, s[2:3]
	v_not_b32_e32 v10, v9
	v_cmp_gt_i64_e64 s[2:3], 0, v[8:9]
	v_sub_u32_e32 v31, 31, v8
	s_nop 0
	v_cndmask_b32_e64 v9, v10, |v9|, s[2:3]
	v_not_b32_e32 v10, v7
	v_cmp_gt_i64_e64 s[2:3], 0, v[6:7]
	s_nop 1
	v_cndmask_b32_e64 v6, v10, |v7|, s[2:3]
	v_not_b32_e32 v7, v5
	v_cmp_gt_i64_e64 s[2:3], 0, v[4:5]
	s_nop 1
	v_cndmask_b32_e64 v4, v7, |v5|, s[2:3]
	v_not_b32_e32 v5, v3
	v_cmp_gt_i64_e64 s[2:3], 0, v[2:3]
	s_nop 1
	v_cndmask_b32_e64 v2, v5, |v3|, s[2:3]
	v_sub_f32_e32 v3, v4, v2
	v_mul_f32_e32 v3, 0x3fb8aa3b, v3
	v_exp_f32_e32 v13, v3
	v_sub_f32_e32 v3, v6, v2
	v_mul_f32_e32 v3, 0x3fb8aa3b, v3
	v_sub_f32_e32 v2, v9, v2
	v_exp_f32_e32 v28, v3
	v_mul_f32_e32 v2, 0x3fb8aa3b, v2
	v_exp_f32_e32 v29, v2
	v_add_f32_e32 v2, 1.0, v13
	v_add_f32_e32 v2, v2, v28
	s_add_i32 s2, 0, 0x20840
	v_add_f32_e32 v2, v2, v29
	v_rcp_f32_e32 v32, v2
	v_add_u32_e32 v2, -3, v26
	v_ashrrev_i32_e32 v3, 31, v2
	v_lshlrev_b64 v[2:3], 2, v[2:3]
	v_lshl_add_u64 v[4:5], s[28:29], 0, v[2:3]
	global_store_dword v[4:5], v30, off
	v_add_u32_e32 v4, -2, v26
	v_ashrrev_i32_e32 v5, 31, v4
	v_lshlrev_b64 v[4:5], 2, v[4:5]
	v_lshl_add_u64 v[6:7], s[28:29], 0, v[4:5]
	global_store_dword v[6:7], v17, off
	v_add_u32_e32 v6, -1, v26
	v_ashrrev_i32_e32 v7, 31, v6
	v_lshlrev_b64 v[6:7], 2, v[6:7]
	v_lshl_add_u64 v[8:9], s[28:29], 0, v[6:7]
	global_store_dword v[8:9], v12, off
	v_lshlrev_b64 v[8:9], 2, v[26:27]
	v_lshl_add_u64 v[10:11], s[28:29], 0, v[8:9]
	v_lshl_add_u64 v[2:3], s[42:43], 0, v[2:3]
	global_store_dword v[10:11], v31, off
	global_store_dword v[2:3], v32, off
	v_mul_f32_e32 v10, v13, v32
	v_lshl_add_u64 v[2:3], s[42:43], 0, v[4:5]
	global_store_dword v[2:3], v10, off
	v_mul_f32_e32 v4, v28, v32
	v_lshl_add_u64 v[2:3], s[42:43], 0, v[6:7]
	global_store_dword v[2:3], v4, off
	v_mul_f32_e32 v4, v29, v32
	v_lshl_add_u64 v[2:3], s[42:43], 0, v[8:9]
	global_store_dword v[2:3], v4, off
	v_lshl_add_u32 v2, v30, 2, s2
	ds_add_u32 v2, v250
	v_lshl_add_u32 v2, v17, 2, s2
	ds_add_u32 v2, v250
	v_lshl_add_u32 v2, v12, 2, s2
	ds_add_u32 v2, v250
	v_lshl_add_u32 v2, v31, 2, s2
	ds_add_u32 v2, v250
	s_branch .LBB0_1417

.LBB0_1583:
	s_andn2_b64 vcc, exec, s[2:3]
	v_mov_b32_e32 v215, v174
	v_mov_b32_e32 v216, v176
	v_mov_b32_e32 v217, v178
	v_mov_b32_e32 v218, v180
	s_cbranch_vccnz .LBB0_1585
	s_lshl_b32 s0, s51, 8
	v_add_u32_e32 v2, s0, v1
	v_ashrrev_i32_e32 v3, 31, v2
	v_lshl_add_u64 v[2:3], v[2:3], 2, s[28:29]
	global_load_dword v68, v[2:3], off
	v_add_u32_e32 v2, s0, v236
	v_ashrrev_i32_e32 v3, 31, v2
	v_lshl_add_u64 v[2:3], v[2:3], 2, s[28:29]
	global_load_dword v69, v[2:3], off
	s_bitset1_b32 s0, 7
	v_add_u32_e32 v2, s0, v1
	v_ashrrev_i32_e32 v3, 31, v2
	v_lshl_add_u64 v[2:3], v[2:3], 2, s[28:29]
	global_load_dword v70, v[2:3], off
	v_add_u32_e32 v2, s0, v236
	v_ashrrev_i32_e32 v3, 31, v2
	v_lshl_add_u64 v[2:3], v[2:3], 2, s[28:29]
	global_load_dword v71, v[2:3], off
	s_waitcnt vmcnt(0)
	v_lshl_add_u32 v215, v68, 10, v219
	v_lshl_add_u32 v216, v69, 10, v212
	v_lshl_add_u32 v217, v70, 10, v219
	v_lshl_add_u32 v218, v71, 10, v212

.LBB0_1731:
	s_add_u32 s0, s84, s6
	s_addc_u32 s1, s85, s7
	s_add_u32 s8, s0, 0x2bc10000
	s_addc_u32 s9, s1, 0
	v_mov_b32_e32 v11, 0x2bc10000
	global_load_dwordx4 v[2:5], v35, s[8:9] offset:16
	global_load_dwordx4 v[36:39], v11, s[0:1]
	v_lshl_add_u64 v[30:31], s[84:85], 0, v[28:29]
	s_mov_b32 s0, 0x178000
	v_add_co_u32_e32 v32, vcc, s0, v30
	v_lshlrev_b32_e32 v11, 1, v10
	s_nop 0
	v_addc_co_u32_e32 v33, vcc, 0, v31, vcc
	global_load_dwordx2 v[40:41], v[32:33], off
	v_lshlrev_b32_e32 v34, 2, v6
	v_lshlrev_b32_e32 v13, 2, v12
	v_lshlrev_b32_e32 v15, 2, v10
	s_waitcnt vmcnt(0)
	v_lshlrev_b32_e32 v76, 16, v40
	v_and_b32_e32 v77, 0xffff0000, v40
	v_lshlrev_b32_e32 v74, 16, v41
	v_and_b32_e32 v75, 0xffff0000, v41
	v_ashrrev_i32_e32 v41, 31, v36
	v_mov_b32_e32 v40, v36
	v_lshlrev_b64 v[40:41], 11, v[40:41]
	v_lshl_add_u64 v[42:43], v[8:9], 0, v[40:41]
	global_load_dwordx2 v[114:115], v[42:43], off
	v_ashrrev_i32_e32 v43, 31, v37
	v_mov_b32_e32 v42, v37
	v_lshlrev_b64 v[36:37], 11, v[42:43]
	v_lshl_add_u64 v[42:43], v[8:9], 0, v[36:37]
	global_load_dwordx2 v[116:117], v[42:43], off
	v_ashrrev_i32_e32 v43, 31, v38
	v_mov_b32_e32 v42, v38
	v_lshlrev_b64 v[42:43], 11, v[42:43]
	v_lshl_add_u64 v[44:45], v[8:9], 0, v[42:43]
	global_load_dwordx2 v[118:119], v[44:45], off
	v_ashrrev_i32_e32 v45, 31, v39
	v_mov_b32_e32 v44, v39
	v_lshl_add_u64 v[36:37], s[4:5], 0, v[36:37]
	v_lshlrev_b64 v[38:39], 11, v[44:45]
	v_readfirstlane_b32 s10, v36
	v_readfirstlane_b32 s11, v37
	v_lshl_add_u64 v[36:37], s[4:5], 0, v[42:43]
	v_lshl_add_u64 v[40:41], s[4:5], 0, v[40:41]
	v_readfirstlane_b32 s14, v36
	v_readfirstlane_b32 s15, v37
	v_lshl_add_u64 v[36:37], s[4:5], 0, v[38:39]
	v_lshl_add_u64 v[44:45], v[8:9], 0, v[38:39]
	v_readfirstlane_b32 s8, v40
	v_readfirstlane_b32 s9, v41
	v_readfirstlane_b32 s16, v36
	v_readfirstlane_b32 s17, v37
	global_load_dwordx2 v[120:121], v[44:45], off
	s_nop 0
	global_load_dwordx2 v[44:45], v[32:33], off offset:512
	global_load_dwordx2 v[106:107], v11, s[8:9]
	global_load_dwordx2 v[108:109], v11, s[10:11]
	global_load_dwordx2 v[110:111], v11, s[14:15]
	global_load_dwordx2 v[112:113], v11, s[16:17]
	global_load_dwordx2 v[36:37], v[32:33], off offset:1024
	s_waitcnt vmcnt(0)
	v_lshlrev_b32_e32 v122, 16, v120
	v_lshlrev_b32_e32 v80, 16, v44
	v_and_b32_e32 v81, 0xffff0000, v44
	v_lshlrev_b32_e32 v78, 16, v45
	v_and_b32_e32 v79, 0xffff0000, v45
	v_lshlrev_b32_e32 v84, 16, v36
	v_and_b32_e32 v85, 0xffff0000, v36
	v_lshlrev_b32_e32 v82, 16, v37
	v_and_b32_e32 v83, 0xffff0000, v37
	global_load_dwordx2 v[104:105], v1, s[8:9]
	global_load_dwordx2 v[102:103], v1, s[10:11]
	global_load_dwordx2 v[100:101], v1, s[14:15]
	global_load_dwordx2 v[90:91], v1, s[16:17]
	global_load_dwordx2 v[36:37], v[32:33], off offset:1536
	global_load_dwordx2 v[98:99], v7, s[8:9]
	global_load_dwordx2 v[96:97], v7, s[10:11]
	global_load_dwordx2 v[94:95], v7, s[14:15]
	global_load_dwordx2 v[92:93], v7, s[16:17]
	global_load_dwordx2 v[66:67], v[32:33], off offset:2048
	v_and_b32_e32 v123, 0xffff0000, v120
	s_waitcnt vmcnt(0)
	v_lshlrev_b32_e32 v86, 16, v36
	v_and_b32_e32 v87, 0xffff0000, v36
	v_lshlrev_b32_e32 v88, 16, v37
	v_and_b32_e32 v89, 0xffff0000, v37
	v_ashrrev_i32_e32 v37, 31, v2
	v_mov_b32_e32 v36, v2
	v_lshlrev_b64 v[36:37], 11, v[36:37]
	v_lshl_add_u64 v[38:39], v[8:9], 0, v[36:37]
	global_load_dwordx2 v[58:59], v[38:39], off
	v_ashrrev_i32_e32 v39, 31, v3
	v_mov_b32_e32 v38, v3
	v_lshlrev_b64 v[2:3], 11, v[38:39]
	v_lshl_add_u64 v[38:39], v[8:9], 0, v[2:3]
	global_load_dwordx2 v[60:61], v[38:39], off
	v_ashrrev_i32_e32 v39, 31, v4
	v_mov_b32_e32 v38, v4
	v_lshlrev_b64 v[38:39], 11, v[38:39]
	v_lshl_add_u64 v[40:41], v[8:9], 0, v[38:39]
	global_load_dwordx2 v[62:63], v[40:41], off
	v_ashrrev_i32_e32 v41, 31, v5
	v_mov_b32_e32 v40, v5
	v_lshl_add_u64 v[2:3], s[4:5], 0, v[2:3]
	v_lshlrev_b64 v[4:5], 11, v[40:41]
	v_readfirstlane_b32 s8, v2
	v_readfirstlane_b32 s9, v3
	v_lshl_add_u64 v[2:3], s[4:5], 0, v[38:39]
	v_lshl_add_u64 v[36:37], s[4:5], 0, v[36:37]
	v_readfirstlane_b32 s10, v2
	v_readfirstlane_b32 s11, v3
	v_lshl_add_u64 v[2:3], s[4:5], 0, v[4:5]
	v_lshl_add_u64 v[40:41], v[8:9], 0, v[4:5]
	v_readfirstlane_b32 s0, v36
	v_readfirstlane_b32 s1, v37
	v_readfirstlane_b32 s14, v2
	v_readfirstlane_b32 s15, v3
	global_load_dwordx2 v[64:65], v[40:41], off
	global_load_dwordx2 v[68:69], v[32:33], off offset:2560
	global_load_dwordx2 v[52:53], v11, s[8:9]
	global_load_dwordx2 v[50:51], v11, s[0:1]
	global_load_dwordx2 v[54:55], v11, s[10:11]
	global_load_dwordx2 v[56:57], v11, s[14:15]
	global_load_dwordx2 v[70:71], v[32:33], off offset:3072
	global_load_dwordx2 v[48:49], v1, s[0:1]
	global_load_dwordx2 v[46:47], v1, s[8:9]
	global_load_dwordx2 v[44:45], v1, s[10:11]
	global_load_dwordx2 v[42:43], v1, s[14:15]
	global_load_dwordx2 v[72:73], v[32:33], off offset:3584
	global_load_dwordx2 v[40:41], v7, s[0:1]
	global_load_dwordx2 v[38:39], v7, s[8:9]
	global_load_dwordx2 v[36:37], v7, s[10:11]
	s_nop 0
	global_load_dwordx2 v[32:33], v7, s[14:15]
	s_ashr_i32 s0, s2, 31
	s_lshr_b32 s0, s0, 20
	s_add_i32 s0, s2, s0
	s_ashr_i32 s0, s0, 12
	s_cmpk_lt_i32 s2, 0x4000
	v_lshlrev_b32_e32 v2, 16, v114
	v_and_b32_e32 v3, 0xffff0000, v114
	v_lshlrev_b32_e32 v4, 16, v116
	v_and_b32_e32 v5, 0xffff0000, v116
	s_cselect_b32 s0, s0, 4
	v_pk_add_f32 v[2:3], v[2:3], v[4:5]
	v_lshlrev_b32_e32 v4, 16, v118
	v_and_b32_e32 v5, 0xffff0000, v118
	s_mul_i32 s10, s0, 0x6000
	v_pk_add_f32 v[4:5], v[4:5], v[122:123]
	s_mul_hi_i32 s3, s0, 0x6000
	s_add_u32 s8, s18, s10
	v_pk_add_f32 v[2:3], v[2:3], v[4:5]
	v_lshlrev_b32_e32 v4, 16, v115
	v_and_b32_e32 v5, 0xffff0000, v115
	v_lshlrev_b32_e32 v114, 16, v117
	v_and_b32_e32 v115, 0xffff0000, v117
	s_addc_u32 s9, s19, s3
	v_pk_add_f32 v[4:5], v[4:5], v[114:115]
	v_lshlrev_b32_e32 v114, 16, v119
	v_and_b32_e32 v115, 0xffff0000, v119
	v_lshlrev_b32_e32 v116, 16, v121
	v_and_b32_e32 v117, 0xffff0000, v121
	v_pk_add_f32 v[114:115], v[114:115], v[116:117]
	v_lshl_add_u64 v[116:117], s[8:9], 0, v[34:35]
	s_mov_b64 s[0:1], 0x5000
	v_pk_add_f32 v[4:5], v[4:5], v[114:115]
	v_lshl_add_u64 v[114:115], v[116:117], 0, s[0:1]
	v_add_co_u32_e32 v116, vcc, s28, v116
	v_readlane_b32 s8, v255, 48
	s_nop 0
	v_addc_co_u32_e32 v117, vcc, 0, v117, vcc
	global_load_dwordx4 v[116:119], v[116:117], off
	global_load_dwordx4 v[124:127], v[114:115], off offset:1024
	global_load_dwordx4 v[128:131], v[114:115], off offset:2048
	global_load_dwordx4 v[132:135], v[114:115], off offset:3072
	v_readlane_b32 s9, v255, 49
	s_mov_b64 s[0:1], -1
	s_and_b64 vcc, exec, s[8:9]
	v_lshlrev_b32_e32 v11, 2, v14
	s_waitcnt vmcnt(0)
	v_pk_fma_f32 v[74:75], v[4:5], v[118:119], v[74:75]
	v_pk_fma_f32 v[76:77], v[2:3], v[116:117], v[76:77]
	v_lshlrev_b32_e32 v2, 16, v106
	v_and_b32_e32 v3, 0xffff0000, v106
	v_lshlrev_b32_e32 v4, 16, v108
	v_and_b32_e32 v5, 0xffff0000, v108
	v_pk_add_f32 v[2:3], v[2:3], v[4:5]
	v_lshlrev_b32_e32 v4, 16, v110
	v_and_b32_e32 v5, 0xffff0000, v110
	v_lshlrev_b32_e32 v116, 16, v112
	v_and_b32_e32 v117, 0xffff0000, v112
	v_pk_add_f32 v[4:5], v[4:5], v[116:117]
	v_lshlrev_b32_e32 v106, 16, v113
	v_pk_add_f32 v[116:117], v[2:3], v[4:5]
	v_lshlrev_b32_e32 v2, 16, v107
	v_and_b32_e32 v3, 0xffff0000, v107
	v_lshlrev_b32_e32 v4, 16, v109
	v_and_b32_e32 v5, 0xffff0000, v109
	v_pk_add_f32 v[2:3], v[2:3], v[4:5]
	v_lshlrev_b32_e32 v4, 16, v111
	v_and_b32_e32 v5, 0xffff0000, v111
	v_and_b32_e32 v107, 0xffff0000, v113
	v_pk_add_f32 v[4:5], v[4:5], v[106:107]
	s_nop 0
	v_pk_add_f32 v[106:107], v[2:3], v[4:5]
	v_mov_b64_e32 v[2:3], v[124:125]
	v_mov_b64_e32 v[4:5], v[126:127]
	s_nop 0
	v_pk_fma_f32 v[78:79], v[106:107], v[4:5], v[78:79]
	v_pk_fma_f32 v[80:81], v[116:117], v[2:3], v[80:81]
	v_lshlrev_b32_e32 v2, 16, v104
	v_and_b32_e32 v3, 0xffff0000, v104
	v_lshlrev_b32_e32 v4, 16, v102
	v_and_b32_e32 v5, 0xffff0000, v102
	v_pk_add_f32 v[2:3], v[2:3], v[4:5]
	v_lshlrev_b32_e32 v4, 16, v100
	v_and_b32_e32 v5, 0xffff0000, v100
	v_lshlrev_b32_e32 v106, 16, v90
	v_and_b32_e32 v107, 0xffff0000, v90
	v_pk_add_f32 v[4:5], v[4:5], v[106:107]
	v_lshlrev_b32_e32 v90, 16, v91
	v_pk_add_f32 v[106:107], v[2:3], v[4:5]
	v_lshlrev_b32_e32 v2, 16, v105
	v_and_b32_e32 v3, 0xffff0000, v105
	v_lshlrev_b32_e32 v4, 16, v103
	v_and_b32_e32 v5, 0xffff0000, v103
	v_pk_add_f32 v[2:3], v[2:3], v[4:5]
	v_lshlrev_b32_e32 v4, 16, v101
	v_and_b32_e32 v5, 0xffff0000, v101
	v_and_b32_e32 v91, 0xffff0000, v91
	v_pk_add_f32 v[4:5], v[4:5], v[90:91]
	s_nop 0
	v_pk_add_f32 v[90:91], v[2:3], v[4:5]
	v_mov_b64_e32 v[2:3], v[128:129]
	v_mov_b64_e32 v[4:5], v[130:131]
	s_nop 0
	v_pk_fma_f32 v[82:83], v[90:91], v[4:5], v[82:83]
	v_pk_fma_f32 v[84:85], v[106:107], v[2:3], v[84:85]
	v_lshlrev_b32_e32 v2, 16, v98
	v_and_b32_e32 v3, 0xffff0000, v98
	v_lshlrev_b32_e32 v4, 16, v96
	v_and_b32_e32 v5, 0xffff0000, v96
	v_pk_add_f32 v[2:3], v[2:3], v[4:5]
	v_lshlrev_b32_e32 v4, 16, v94
	v_and_b32_e32 v5, 0xffff0000, v94
	v_lshlrev_b32_e32 v90, 16, v92
	v_and_b32_e32 v91, 0xffff0000, v92
	v_pk_add_f32 v[4:5], v[4:5], v[90:91]
	v_lshlrev_b32_e32 v92, 16, v93
	v_pk_add_f32 v[90:91], v[2:3], v[4:5]
	v_lshlrev_b32_e32 v2, 16, v99
	v_and_b32_e32 v3, 0xffff0000, v99
	v_lshlrev_b32_e32 v4, 16, v97
	v_and_b32_e32 v5, 0xffff0000, v97
	v_pk_add_f32 v[2:3], v[2:3], v[4:5]
	v_lshlrev_b32_e32 v4, 16, v95
	v_and_b32_e32 v5, 0xffff0000, v95
	v_and_b32_e32 v93, 0xffff0000, v93
	v_pk_add_f32 v[4:5], v[4:5], v[92:93]
	v_pk_mul_f32 v[96:97], v[76:77], v[76:77]
	v_pk_add_f32 v[92:93], v[2:3], v[4:5]
	v_mov_b64_e32 v[2:3], v[132:133]
	v_mov_b64_e32 v[4:5], v[134:135]
	v_pk_mul_f32 v[94:95], v[80:81], v[80:81]
	s_nop 0
	v_pk_fma_f32 v[88:89], v[92:93], v[4:5], v[88:89]
	v_pk_fma_f32 v[86:87], v[90:91], v[2:3], v[86:87]
	v_mul_f32_e32 v4, v88, v88
	v_mul_f32_e32 v92, v86, v86
	v_mul_f32_e32 v90, v87, v87
	v_mul_f32_e32 v2, v89, v89
	s_cbranch_vccz .LBB0_1733
	s_mov_b64 s[0:1], 0x178000
	v_lshl_add_u64 v[98:99], v[30:31], 0, s[0:1]
	s_mov_b64 s[0:1], 0x178200
	v_cvt_pk_bf16_f32 v106, v76, v77
	v_cvt_pk_bf16_f32 v107, v74, v75
	v_lshl_add_u64 v[100:101], v[30:31], 0, s[0:1]
	s_mov_b64 s[0:1], 0x178400
	global_store_dwordx2 v[98:99], v[106:107], off
	v_cvt_pk_bf16_f32 v98, v80, v81
	v_cvt_pk_bf16_f32 v99, v78, v79
	v_lshl_add_u64 v[102:103], v[30:31], 0, s[0:1]
	s_mov_b64 s[0:1], 0x178600
	global_store_dwordx2 v[100:101], v[98:99], off
	v_cvt_pk_bf16_f32 v98, v84, v85
	v_cvt_pk_bf16_f32 v99, v82, v83
	v_lshl_add_u64 v[104:105], v[30:31], 0, s[0:1]
	global_store_dwordx2 v[102:103], v[98:99], off
	v_cvt_pk_bf16_f32 v98, v86, v87
	v_cvt_pk_bf16_f32 v99, v88, v89
	global_store_dwordx2 v[104:105], v[98:99], off
	v_pk_mul_f32 v[98:99], v[74:75], v[74:75]
	v_mov_b32_e32 v100, v96
	v_mov_b32_e32 v101, v99
	v_pk_mov_b32 v[98:99], v[96:97], v[98:99] op_sel:[1,0]
	s_add_u32 s8, s22, s10
	v_pk_add_f32 v[98:99], v[98:99], v[100:101]
	v_mov_b32_e32 v100, v94
	v_pk_add_f32 v[110:111], v[98:99], v[98:99] op_sel_hi:[0,1]
	v_pk_mul_f32 v[98:99], v[78:79], v[78:79]
	s_addc_u32 s9, s23, s3
	v_mov_b32_e32 v101, v99
	v_pk_mov_b32 v[98:99], v[94:95], v[98:99] op_sel:[1,0]
	s_add_u32 s10, s8, 0x1000
	v_pk_add_f32 v[98:99], v[98:99], v[100:101]
	s_addc_u32 s11, s9, 0
	v_pk_add_f32 v[112:113], v[98:99], v[98:99] op_sel_hi:[0,1]
	v_mul_f32_e32 v98, v84, v84
	v_pk_fma_f32 v[114:115], v[84:85], v[84:85], v[98:99] op_sel_hi:[1,1,0]
	v_mul_f32_e32 v98, v82, v82
	v_pk_fma_f32 v[116:117], v[82:83], v[82:83], v[98:99] op_sel_hi:[1,1,0]
	global_load_dwordx4 v[98:101], v[16:17], off
	global_load_dwordx4 v[102:105], v34, s[8:9]
	global_load_dwordx4 v[106:109], v34, s[10:11]
	global_load_dwordx4 v[136:139], v[18:19], off
	global_load_dwordx4 v[140:143], v15, s[10:11]
	global_load_dwordx4 v[144:147], v34, s[8:9] offset:1024
	global_load_dwordx4 v[148:151], v[20:21], off
	global_load_dwordx4 v[152:155], v13, s[10:11]
	global_load_dwordx4 v[156:159], v34, s[8:9] offset:2048
	global_load_dwordx4 v[172:175], v[22:23], off
	global_load_dwordx4 v[176:179], v11, s[10:11]
	global_load_dwordx4 v[180:183], v34, s[8:9] offset:3072
	v_mov_b32_e32 v5, v111
	v_mov_b32_e32 v3, v113
	v_mov_b32_e32 v93, v115
	v_mov_b32_e32 v91, v117
	v_pk_add_f32 v[110:111], v[4:5], v[2:3]
	v_and_b32_e32 v5, 64, v203
	v_pk_add_f32 v[114:115], v[92:93], v[90:91]
	v_add_u32_e32 v5, 64, v5
	v_xor_b32_e32 v91, 1, v203
	v_cmp_lt_i32_e32 vcc, v91, v5
	v_pk_add_f32 v[110:111], v[114:115], v[110:111]
	s_mov_b32 s0, 0x4578000
	v_cndmask_b32_e32 v91, v203, v91, vcc
	v_add_f32_e32 v3, v110, v111
	v_lshlrev_b32_e32 v91, 2, v91
	s_nop 1
	v_mov_b32_dpp v91, v3 quad_perm:[1,0,3,2] row_mask:0xf bank_mask:0xf
	s_waitcnt lgkmcnt(0)
	v_add_f32_e32 v3, v3, v91
	v_xor_b32_e32 v91, 2, v203
	v_cmp_lt_i32_e32 vcc, v91, v5
	s_waitcnt vmcnt(0)
	v_pk_add_f32 v[108:109], v[108:109], 1.0 op_sel_hi:[1,0]
	v_cndmask_b32_e32 v91, v203, v91, vcc
	v_lshlrev_b32_e32 v91, 2, v91
	s_nop 1
	v_mov_b32_dpp v91, v3 quad_perm:[2,3,0,1] row_mask:0xf bank_mask:0xf
	v_pk_add_f32 v[106:107], v[106:107], 1.0 op_sel_hi:[1,0]
	s_waitcnt lgkmcnt(0)
	v_add_f32_e32 v3, v3, v91
	v_xor_b32_e32 v91, 4, v203
	v_cmp_lt_i32_e32 vcc, v91, v5
	s_nop 1
	v_cndmask_b32_e32 v91, v203, v91, vcc
	v_lshlrev_b32_e32 v91, 2, v91
	s_nop 1
	v_mov_b32_dpp v91, v3 row_half_mirror row_mask:0xf bank_mask:0xf
	s_waitcnt lgkmcnt(0)
	v_add_f32_e32 v3, v3, v91
	v_xor_b32_e32 v91, 8, v203
	v_cmp_lt_i32_e32 vcc, v91, v5
	s_nop 1
	v_cndmask_b32_e32 v91, v203, v91, vcc
	v_lshlrev_b32_e32 v91, 2, v91
	s_nop 1
	v_mov_b32_dpp v91, v3 row_mirror row_mask:0xf bank_mask:0xf
	s_waitcnt lgkmcnt(0)
	v_add_f32_e32 v3, v3, v91
	v_xor_b32_e32 v91, 16, v203
	v_cmp_lt_i32_e32 vcc, v91, v5
	s_nop 1
	v_cndmask_b32_e32 v91, v203, v91, vcc
	v_lshlrev_b32_e32 v91, 2, v91
	v_mov_b32_e32 v91, v3
	s_nop 1
	v_permlane16_swap_b32_e32 v91, v3
	s_waitcnt lgkmcnt(0)
	v_add_f32_e32 v3, v3, v91
	v_xor_b32_e32 v91, 32, v203
	v_cmp_lt_i32_e32 vcc, v91, v5
	s_nop 1
	v_cndmask_b32_e32 v5, v203, v91, vcc
	v_lshlrev_b32_e32 v5, 2, v5
	v_mov_b32_e32 v5, v3
	s_nop 1
	v_permlane32_swap_b32_e32 v5, v3
	s_waitcnt lgkmcnt(0)
	v_add_f32_e32 v3, v3, v5
	v_fmamk_f32 v3, v3, 0x3a800000, v165
	v_rsq_f32_e32 v110, v3
	s_nop 0
	v_pk_mul_f32 v[112:113], v[74:75], v[110:111] op_sel_hi:[1,0]
	v_pk_mul_f32 v[114:115], v[76:77], v[110:111] op_sel_hi:[1,0]
	v_pk_mul_f32 v[100:101], v[100:101], v[112:113]
	v_pk_mul_f32 v[98:99], v[98:99], v[114:115]
	v_pk_fma_f32 v[100:101], v[108:109], v[100:101], v[104:105]
	v_pk_fma_f32 v[98:99], v[106:107], v[98:99], v[102:103]
	v_add_co_u32_e32 v112, vcc, s0, v30
	v_cvt_pk_bf16_f32 v98, v98, v99
	v_cvt_pk_bf16_f32 v99, v100, v101
	v_addc_co_u32_e32 v113, vcc, 0, v31, vcc
	global_store_dwordx2 v[112:113], v[98:99], off
	v_mov_b64_e32 v[98:99], v[136:137]
	v_mov_b64_e32 v[100:101], v[138:139]
	v_mov_b64_e32 v[102:103], v[140:141]
	v_mov_b64_e32 v[104:105], v[142:143]
	v_mov_b64_e32 v[106:107], v[144:145]
	v_mov_b64_e32 v[108:109], v[146:147]
	s_nop 0
	s_nop 0
	s_nop 0
	v_pk_mul_f32 v[114:115], v[78:79], v[110:111] op_sel_hi:[1,0]
	v_pk_mul_f32 v[116:117], v[80:81], v[110:111] op_sel_hi:[1,0]
	s_mov_b64 s[0:1], 0
	s_nop 0
	v_pk_mul_f32 v[98:99], v[98:99], v[116:117]
	v_pk_mul_f32 v[100:101], v[100:101], v[114:115]
	s_nop 0
	v_pk_add_f32 v[104:105], v[104:105], 1.0 op_sel_hi:[1,0]
	v_pk_add_f32 v[102:103], v[102:103], 1.0 op_sel_hi:[1,0]
	s_nop 0
	v_pk_fma_f32 v[100:101], v[104:105], v[100:101], v[108:109]
	v_pk_fma_f32 v[98:99], v[102:103], v[98:99], v[106:107]
	v_pk_mul_f32 v[114:115], v[82:83], v[110:111] op_sel_hi:[1,0]
	v_cvt_pk_bf16_f32 v98, v98, v99
	v_cvt_pk_bf16_f32 v99, v100, v101
	global_store_dwordx2 v[112:113], v[98:99], off offset:512
	v_mov_b64_e32 v[98:99], v[148:149]
	v_mov_b64_e32 v[100:101], v[150:151]
	v_mov_b64_e32 v[102:103], v[152:153]
	v_mov_b64_e32 v[104:105], v[154:155]
	v_mov_b64_e32 v[106:107], v[156:157]
	v_mov_b64_e32 v[108:109], v[158:159]
	s_nop 0
	s_nop 0
	s_nop 0
	v_pk_mul_f32 v[116:117], v[84:85], v[110:111] op_sel_hi:[1,0]
	s_nop 0
	v_pk_mul_f32 v[100:101], v[114:115], v[100:101]
	v_pk_mul_f32 v[98:99], v[116:117], v[98:99]
	s_nop 0
	v_pk_add_f32 v[104:105], v[104:105], 1.0 op_sel_hi:[1,0]
	v_pk_add_f32 v[102:103], v[102:103], 1.0 op_sel_hi:[1,0]
	s_nop 0
	v_pk_fma_f32 v[100:101], v[100:101], v[104:105], v[108:109]
	v_pk_fma_f32 v[98:99], v[98:99], v[102:103], v[106:107]
	v_pk_mul_f32 v[114:115], v[88:89], v[110:111] op_sel_hi:[1,0]
	v_cvt_pk_bf16_f32 v98, v98, v99
	v_cvt_pk_bf16_f32 v99, v100, v101
	global_store_dwordx2 v[112:113], v[98:99], off offset:1024
	v_mov_b64_e32 v[98:99], v[172:173]
	v_mov_b64_e32 v[100:101], v[174:175]
	v_mov_b64_e32 v[102:103], v[176:177]
	v_mov_b64_e32 v[104:105], v[178:179]
	v_mov_b64_e32 v[106:107], v[180:181]
	v_mov_b64_e32 v[108:109], v[182:183]
	s_nop 0
	s_nop 0
	s_nop 0
	v_pk_mul_f32 v[110:111], v[86:87], v[110:111] op_sel_hi:[1,0]
	s_nop 0
	v_pk_mul_f32 v[100:101], v[114:115], v[100:101]
	v_pk_mul_f32 v[98:99], v[110:111], v[98:99]
	s_nop 0
	v_pk_add_f32 v[104:105], v[104:105], 1.0 op_sel_hi:[1,0]
	v_pk_add_f32 v[102:103], v[102:103], 1.0 op_sel_hi:[1,0]
	s_nop 0
	v_pk_fma_f32 v[100:101], v[100:101], v[104:105], v[108:109]
	v_pk_fma_f32 v[98:99], v[98:99], v[102:103], v[106:107]
	s_nop 0
	v_cvt_pk_bf16_f32 v98, v98, v99
	v_cvt_pk_bf16_f32 v99, v100, v101
	global_store_dwordx2 v[112:113], v[98:99], off offset:1536

.LBB0_1735:
	s_add_i32 s0, s2, 1
	s_ashr_i32 s1, s0, 31
	s_lshr_b32 s1, s1, 20
	s_add_i32 s1, s0, s1
	s_ashr_i32 s1, s1, 12
	v_lshlrev_b32_e32 v78, 16, v66
	v_and_b32_e32 v79, 0xffff0000, v66
	v_lshlrev_b32_e32 v80, 16, v67
	v_and_b32_e32 v81, 0xffff0000, v67
	v_lshlrev_b32_e32 v74, 16, v68
	v_and_b32_e32 v75, 0xffff0000, v68
	v_lshlrev_b32_e32 v76, 16, v69
	v_and_b32_e32 v77, 0xffff0000, v69
	v_lshlrev_b32_e32 v66, 16, v72
	v_and_b32_e32 v67, 0xffff0000, v72
	v_lshlrev_b32_e32 v68, 16, v73
	v_and_b32_e32 v69, 0xffff0000, v73
	s_cmpk_lt_i32 s0, 0x4000
	v_lshlrev_b32_e32 v2, 16, v58
	v_and_b32_e32 v3, 0xffff0000, v58
	v_lshlrev_b32_e32 v72, 16, v60
	v_and_b32_e32 v73, 0xffff0000, v60
	s_cselect_b32 s0, s1, 4
	v_pk_add_f32 v[2:3], v[2:3], v[72:73]
	v_lshlrev_b32_e32 v72, 16, v62
	v_and_b32_e32 v73, 0xffff0000, v62
	v_lshlrev_b32_e32 v82, 16, v64
	v_and_b32_e32 v83, 0xffff0000, v64
	s_mul_i32 s10, s0, 0x6000
	v_pk_add_f32 v[72:73], v[72:73], v[82:83]
	s_mul_hi_i32 s3, s0, 0x6000
	s_add_u32 s8, s18, s10
	v_pk_add_f32 v[72:73], v[2:3], v[72:73]
	v_lshlrev_b32_e32 v2, 16, v59
	v_and_b32_e32 v3, 0xffff0000, v59
	v_lshlrev_b32_e32 v58, 16, v61
	v_and_b32_e32 v59, 0xffff0000, v61
	s_addc_u32 s9, s19, s3
	v_pk_add_f32 v[2:3], v[2:3], v[58:59]
	v_lshlrev_b32_e32 v58, 16, v63
	v_and_b32_e32 v59, 0xffff0000, v63
	v_lshlrev_b32_e32 v60, 16, v65
	v_and_b32_e32 v61, 0xffff0000, v65
	v_pk_add_f32 v[58:59], v[58:59], v[60:61]
	v_lshl_add_u64 v[60:61], s[8:9], 0, v[34:35]
	s_mov_b64 s[0:1], 0x5000
	v_pk_add_f32 v[58:59], v[2:3], v[58:59]
	v_lshl_add_u64 v[2:3], v[60:61], 0, s[0:1]
	v_add_co_u32_e32 v60, vcc, s28, v60
	v_lshlrev_b32_e32 v64, 16, v52
	s_nop 0
	v_addc_co_u32_e32 v61, vcc, 0, v61, vcc
	global_load_dwordx4 v[60:63], v[60:61], off
	global_load_dwordx4 v[124:127], v[2:3], off offset:1024
	global_load_dwordx4 v[128:131], v[2:3], off offset:2048
	global_load_dwordx4 v[132:135], v[2:3], off offset:3072
	v_and_b32_e32 v65, 0xffff0000, v52
	v_lshlrev_b32_e32 v52, 16, v53
	v_and_b32_e32 v53, 0xffff0000, v53
	v_lshlrev_b32_e32 v4, 16, v70
	v_and_b32_e32 v5, 0xffff0000, v70
	v_lshlrev_b32_e32 v70, 16, v71
	v_and_b32_e32 v71, 0xffff0000, v71
	v_readlane_b32 s8, v255, 48
	v_readlane_b32 s9, v255, 49
	s_mov_b64 s[0:1], -1
	s_and_b64 vcc, exec, s[8:9]
	s_waitcnt vmcnt(0)
	v_pk_fma_f32 v[58:59], v[58:59], v[62:63], v[80:81]
	v_lshlrev_b32_e32 v62, 16, v50
	v_and_b32_e32 v63, 0xffff0000, v50
	v_lshlrev_b32_e32 v50, 16, v51
	v_and_b32_e32 v51, 0xffff0000, v51
	v_pk_add_f32 v[62:63], v[62:63], v[64:65]
	v_lshlrev_b32_e32 v64, 16, v54
	v_and_b32_e32 v65, 0xffff0000, v54
	v_pk_add_f32 v[50:51], v[50:51], v[52:53]
	v_lshlrev_b32_e32 v52, 16, v55
	v_and_b32_e32 v53, 0xffff0000, v55
	v_lshlrev_b32_e32 v54, 16, v57
	v_and_b32_e32 v55, 0xffff0000, v57
	v_pk_add_f32 v[52:53], v[52:53], v[54:55]
	v_pk_fma_f32 v[60:61], v[72:73], v[60:61], v[78:79]
	v_pk_add_f32 v[50:51], v[50:51], v[52:53]
	v_mov_b64_e32 v[52:53], v[124:125]
	v_mov_b64_e32 v[54:55], v[126:127]
	v_lshlrev_b32_e32 v72, 16, v56
	v_and_b32_e32 v73, 0xffff0000, v56
	v_pk_add_f32 v[64:65], v[64:65], v[72:73]
	v_lshlrev_b32_e32 v56, 16, v46
	v_pk_add_f32 v[62:63], v[62:63], v[64:65]
	v_and_b32_e32 v57, 0xffff0000, v46
	v_lshlrev_b32_e32 v46, 16, v47
	v_and_b32_e32 v47, 0xffff0000, v47
	s_nop 0
	v_pk_fma_f32 v[50:51], v[50:51], v[54:55], v[76:77]
	v_lshlrev_b32_e32 v54, 16, v48
	v_and_b32_e32 v55, 0xffff0000, v48
	v_pk_fma_f32 v[52:53], v[62:63], v[52:53], v[74:75]
	v_pk_add_f32 v[54:55], v[54:55], v[56:57]
	v_lshlrev_b32_e32 v56, 16, v44
	v_and_b32_e32 v57, 0xffff0000, v44
	v_lshlrev_b32_e32 v62, 16, v42
	v_and_b32_e32 v63, 0xffff0000, v42
	v_lshlrev_b32_e32 v48, 16, v49
	v_and_b32_e32 v49, 0xffff0000, v49
	v_lshlrev_b32_e32 v44, 16, v45
	v_and_b32_e32 v45, 0xffff0000, v45
	v_lshlrev_b32_e32 v42, 16, v43
	v_and_b32_e32 v43, 0xffff0000, v43
	v_pk_add_f32 v[46:47], v[48:49], v[46:47]
	v_pk_add_f32 v[42:43], v[44:45], v[42:43]
	v_pk_add_f32 v[56:57], v[56:57], v[62:63]
	v_pk_add_f32 v[42:43], v[46:47], v[42:43]
	v_mov_b64_e32 v[44:45], v[128:129]
	v_mov_b64_e32 v[46:47], v[130:131]
	v_pk_add_f32 v[54:55], v[54:55], v[56:57]
	v_lshlrev_b32_e32 v48, 16, v32
	v_and_b32_e32 v49, 0xffff0000, v32
	v_lshlrev_b32_e32 v32, 16, v33
	v_and_b32_e32 v33, 0xffff0000, v33
	s_nop 0
	v_pk_fma_f32 v[42:43], v[42:43], v[46:47], v[70:71]
	v_pk_fma_f32 v[44:45], v[54:55], v[44:45], v[4:5]
	v_lshlrev_b32_e32 v4, 16, v40
	v_and_b32_e32 v5, 0xffff0000, v40
	v_lshlrev_b32_e32 v46, 16, v38
	v_and_b32_e32 v47, 0xffff0000, v38
	v_pk_add_f32 v[4:5], v[4:5], v[46:47]
	v_lshlrev_b32_e32 v46, 16, v36
	v_and_b32_e32 v47, 0xffff0000, v36
	v_pk_add_f32 v[46:47], v[46:47], v[48:49]
	v_lshlrev_b32_e32 v38, 16, v39
	v_pk_add_f32 v[46:47], v[4:5], v[46:47]
	v_lshlrev_b32_e32 v4, 16, v41
	v_and_b32_e32 v5, 0xffff0000, v41
	v_and_b32_e32 v39, 0xffff0000, v39
	v_lshlrev_b32_e32 v36, 16, v37
	v_and_b32_e32 v37, 0xffff0000, v37
	v_pk_add_f32 v[4:5], v[4:5], v[38:39]
	v_pk_add_f32 v[32:33], v[36:37], v[32:33]
	v_pk_mul_f32 v[48:49], v[60:61], v[60:61]
	v_pk_add_f32 v[32:33], v[4:5], v[32:33]
	v_mov_b64_e32 v[2:3], v[132:133]
	v_mov_b64_e32 v[4:5], v[134:135]
	s_nop 0
	v_pk_fma_f32 v[32:33], v[32:33], v[4:5], v[68:69]
	v_pk_fma_f32 v[36:37], v[46:47], v[2:3], v[66:67]
	v_mul_f32_e32 v4, v32, v32
	v_mul_f32_e32 v40, v36, v36
	v_mul_f32_e32 v38, v37, v37
	v_mul_f32_e32 v2, v33, v33
	v_pk_mul_f32 v[46:47], v[52:53], v[52:53]
	s_cbranch_vccz .LBB0_1737
	s_mov_b64 s[0:1], 0x178800
	v_lshl_add_u64 v[54:55], v[30:31], 0, s[0:1]
	s_mov_b64 s[0:1], 0x178a00
	v_cvt_pk_bf16_f32 v66, v60, v61
	v_cvt_pk_bf16_f32 v67, v58, v59
	v_lshl_add_u64 v[56:57], v[30:31], 0, s[0:1]
	s_mov_b64 s[0:1], 0x178c00
	global_store_dwordx2 v[54:55], v[66:67], off
	v_cvt_pk_bf16_f32 v54, v52, v53
	v_cvt_pk_bf16_f32 v55, v50, v51
	v_lshl_add_u64 v[62:63], v[30:31], 0, s[0:1]
	s_mov_b64 s[0:1], 0x178e00
	global_store_dwordx2 v[56:57], v[54:55], off
	v_cvt_pk_bf16_f32 v54, v44, v45
	v_cvt_pk_bf16_f32 v55, v42, v43
	v_lshl_add_u64 v[64:65], v[30:31], 0, s[0:1]
	global_store_dwordx2 v[62:63], v[54:55], off
	v_cvt_pk_bf16_f32 v54, v36, v37
	v_cvt_pk_bf16_f32 v55, v32, v33
	global_store_dwordx2 v[64:65], v[54:55], off
	v_pk_mul_f32 v[54:55], v[58:59], v[58:59]
	v_mov_b32_e32 v56, v48
	v_mov_b32_e32 v57, v55
	v_pk_mov_b32 v[54:55], v[48:49], v[54:55] op_sel:[1,0]
	s_add_u32 s8, s22, s10
	v_pk_add_f32 v[54:55], v[54:55], v[56:57]
	v_mov_b32_e32 v56, v46
	v_pk_add_f32 v[70:71], v[54:55], v[54:55] op_sel_hi:[0,1]
	v_pk_mul_f32 v[54:55], v[50:51], v[50:51]
	s_addc_u32 s9, s23, s3
	v_mov_b32_e32 v57, v55
	v_pk_mov_b32 v[54:55], v[46:47], v[54:55] op_sel:[1,0]
	s_add_u32 s10, s8, 0x1000
	v_pk_add_f32 v[54:55], v[54:55], v[56:57]
	s_addc_u32 s11, s9, 0
	v_pk_add_f32 v[72:73], v[54:55], v[54:55] op_sel_hi:[0,1]
	v_mul_f32_e32 v54, v44, v44
	v_pk_fma_f32 v[74:75], v[44:45], v[44:45], v[54:55] op_sel_hi:[1,1,0]
	v_mul_f32_e32 v54, v42, v42
	v_pk_fma_f32 v[76:77], v[42:43], v[42:43], v[54:55] op_sel_hi:[1,1,0]
	global_load_dwordx4 v[54:57], v[16:17], off
	global_load_dwordx4 v[62:65], v34, s[8:9]
	global_load_dwordx4 v[66:69], v34, s[10:11]
	global_load_dwordx4 v[136:139], v[18:19], off
	global_load_dwordx4 v[140:143], v15, s[10:11]
	global_load_dwordx4 v[144:147], v34, s[8:9] offset:1024
	global_load_dwordx4 v[148:151], v[20:21], off
	global_load_dwordx4 v[152:155], v13, s[10:11]
	global_load_dwordx4 v[156:159], v34, s[8:9] offset:2048
	global_load_dwordx4 v[172:175], v[22:23], off
	global_load_dwordx4 v[176:179], v11, s[10:11]
	global_load_dwordx4 v[180:183], v34, s[8:9] offset:3072
	v_mov_b32_e32 v5, v71
	v_mov_b32_e32 v3, v73
	v_mov_b32_e32 v41, v75
	v_mov_b32_e32 v39, v77
	v_pk_add_f32 v[70:71], v[4:5], v[2:3]
	v_and_b32_e32 v5, 64, v203
	v_pk_add_f32 v[74:75], v[40:41], v[38:39]
	v_add_u32_e32 v5, 64, v5
	v_xor_b32_e32 v39, 1, v203
	v_cmp_lt_i32_e32 vcc, v39, v5
	v_pk_add_f32 v[70:71], v[74:75], v[70:71]
	s_mov_b32 s0, 0x4578000
	v_cndmask_b32_e32 v39, v203, v39, vcc
	v_add_f32_e32 v3, v70, v71
	v_lshlrev_b32_e32 v39, 2, v39
	s_nop 1
	v_mov_b32_dpp v39, v3 quad_perm:[1,0,3,2] row_mask:0xf bank_mask:0xf
	s_waitcnt lgkmcnt(0)
	v_add_f32_e32 v3, v3, v39
	v_xor_b32_e32 v39, 2, v203
	v_cmp_lt_i32_e32 vcc, v39, v5
	s_waitcnt vmcnt(0)
	v_pk_add_f32 v[68:69], v[68:69], 1.0 op_sel_hi:[1,0]
	v_cndmask_b32_e32 v39, v203, v39, vcc
	v_lshlrev_b32_e32 v39, 2, v39
	s_nop 1
	v_mov_b32_dpp v39, v3 quad_perm:[2,3,0,1] row_mask:0xf bank_mask:0xf
	v_pk_add_f32 v[66:67], v[66:67], 1.0 op_sel_hi:[1,0]
	s_waitcnt lgkmcnt(0)
	v_add_f32_e32 v3, v3, v39
	v_xor_b32_e32 v39, 4, v203
	v_cmp_lt_i32_e32 vcc, v39, v5
	s_nop 1
	v_cndmask_b32_e32 v39, v203, v39, vcc
	v_lshlrev_b32_e32 v39, 2, v39
	s_nop 1
	v_mov_b32_dpp v39, v3 row_half_mirror row_mask:0xf bank_mask:0xf
	s_waitcnt lgkmcnt(0)
	v_add_f32_e32 v3, v3, v39
	v_xor_b32_e32 v39, 8, v203
	v_cmp_lt_i32_e32 vcc, v39, v5
	s_nop 1
	v_cndmask_b32_e32 v39, v203, v39, vcc
	v_lshlrev_b32_e32 v39, 2, v39
	s_nop 1
	v_mov_b32_dpp v39, v3 row_mirror row_mask:0xf bank_mask:0xf
	s_waitcnt lgkmcnt(0)
	v_add_f32_e32 v3, v3, v39
	v_xor_b32_e32 v39, 16, v203
	v_cmp_lt_i32_e32 vcc, v39, v5
	s_nop 1
	v_cndmask_b32_e32 v39, v203, v39, vcc
	v_lshlrev_b32_e32 v39, 2, v39
	v_mov_b32_e32 v39, v3
	s_nop 1
	v_permlane16_swap_b32_e32 v39, v3
	s_waitcnt lgkmcnt(0)
	v_add_f32_e32 v3, v3, v39
	v_xor_b32_e32 v39, 32, v203
	v_cmp_lt_i32_e32 vcc, v39, v5
	s_nop 1
	v_cndmask_b32_e32 v5, v203, v39, vcc
	v_lshlrev_b32_e32 v5, 2, v5
	v_mov_b32_e32 v5, v3
	s_nop 1
	v_permlane32_swap_b32_e32 v5, v3
	v_add_co_u32_e32 v30, vcc, s0, v30
	s_mov_b64 s[0:1], 0
	s_nop 0
	v_addc_co_u32_e32 v31, vcc, 0, v31, vcc
	s_waitcnt lgkmcnt(0)
	v_add_f32_e32 v3, v3, v5
	v_fmamk_f32 v3, v3, 0x3a800000, v165
	v_rsq_f32_e32 v70, v3
	s_nop 0
	v_pk_mul_f32 v[72:73], v[58:59], v[70:71] op_sel_hi:[1,0]
	v_pk_mul_f32 v[74:75], v[60:61], v[70:71] op_sel_hi:[1,0]
	v_pk_mul_f32 v[56:57], v[56:57], v[72:73]
	v_pk_mul_f32 v[54:55], v[54:55], v[74:75]
	v_pk_fma_f32 v[56:57], v[68:69], v[56:57], v[64:65]
	v_pk_fma_f32 v[54:55], v[66:67], v[54:55], v[62:63]
	v_pk_mul_f32 v[72:73], v[50:51], v[70:71] op_sel_hi:[1,0]
	v_cvt_pk_bf16_f32 v54, v54, v55
	v_cvt_pk_bf16_f32 v55, v56, v57
	global_store_dwordx2 v[30:31], v[54:55], off offset:2048
	v_mov_b64_e32 v[54:55], v[136:137]
	v_mov_b64_e32 v[56:57], v[138:139]
	v_mov_b64_e32 v[62:63], v[140:141]
	v_mov_b64_e32 v[64:65], v[142:143]
	v_mov_b64_e32 v[66:67], v[144:145]
	v_mov_b64_e32 v[68:69], v[146:147]
	s_nop 0
	s_nop 0
	s_nop 0
	v_pk_mul_f32 v[74:75], v[52:53], v[70:71] op_sel_hi:[1,0]
	s_nop 0
	v_pk_mul_f32 v[56:57], v[56:57], v[72:73]
	v_pk_mul_f32 v[54:55], v[54:55], v[74:75]
	s_nop 0
	v_pk_add_f32 v[64:65], v[64:65], 1.0 op_sel_hi:[1,0]
	v_pk_add_f32 v[62:63], v[62:63], 1.0 op_sel_hi:[1,0]
	s_nop 0
	v_pk_fma_f32 v[56:57], v[64:65], v[56:57], v[68:69]
	v_pk_fma_f32 v[54:55], v[62:63], v[54:55], v[66:67]
	v_pk_mul_f32 v[72:73], v[42:43], v[70:71] op_sel_hi:[1,0]
	v_cvt_pk_bf16_f32 v54, v54, v55
	v_cvt_pk_bf16_f32 v55, v56, v57
	global_store_dwordx2 v[30:31], v[54:55], off offset:2560
	v_mov_b64_e32 v[54:55], v[148:149]
	v_mov_b64_e32 v[56:57], v[150:151]
	v_mov_b64_e32 v[62:63], v[152:153]
	v_mov_b64_e32 v[64:65], v[154:155]
	v_mov_b64_e32 v[66:67], v[156:157]
	v_mov_b64_e32 v[68:69], v[158:159]
	s_nop 0
	s_nop 0
	s_nop 0
	v_pk_mul_f32 v[74:75], v[44:45], v[70:71] op_sel_hi:[1,0]
	s_nop 0
	v_pk_mul_f32 v[56:57], v[72:73], v[56:57]
	v_pk_mul_f32 v[54:55], v[74:75], v[54:55]
	s_nop 0
	v_pk_add_f32 v[64:65], v[64:65], 1.0 op_sel_hi:[1,0]
	v_pk_add_f32 v[62:63], v[62:63], 1.0 op_sel_hi:[1,0]
	s_nop 0
	v_pk_fma_f32 v[56:57], v[56:57], v[64:65], v[68:69]
	v_pk_fma_f32 v[54:55], v[54:55], v[62:63], v[66:67]
	v_pk_mul_f32 v[72:73], v[32:33], v[70:71] op_sel_hi:[1,0]
	v_cvt_pk_bf16_f32 v54, v54, v55
	v_cvt_pk_bf16_f32 v55, v56, v57
	global_store_dwordx2 v[30:31], v[54:55], off offset:3072
	v_mov_b64_e32 v[54:55], v[172:173]
	v_mov_b64_e32 v[56:57], v[174:175]
	v_mov_b64_e32 v[62:63], v[176:177]
	v_mov_b64_e32 v[64:65], v[178:179]
	v_mov_b64_e32 v[66:67], v[180:181]
	v_mov_b64_e32 v[68:69], v[182:183]
	s_nop 0
	s_nop 0
	s_nop 0
	v_pk_mul_f32 v[70:71], v[36:37], v[70:71] op_sel_hi:[1,0]
	s_nop 0
	v_pk_mul_f32 v[56:57], v[72:73], v[56:57]
	v_pk_mul_f32 v[54:55], v[70:71], v[54:55]
	s_nop 0
	v_pk_add_f32 v[64:65], v[64:65], 1.0 op_sel_hi:[1,0]
	v_pk_add_f32 v[62:63], v[62:63], 1.0 op_sel_hi:[1,0]
	s_nop 0
	v_pk_fma_f32 v[56:57], v[56:57], v[64:65], v[68:69]
	v_pk_fma_f32 v[54:55], v[54:55], v[62:63], v[66:67]
	s_nop 0
	v_cvt_pk_bf16_f32 v54, v54, v55
	v_cvt_pk_bf16_f32 v55, v56, v57
	global_store_dwordx2 v[30:31], v[54:55], off offset:3584
